# speedup vs baseline: 1.0377x; 1.0377x over previous
_Z9ssim_mainPKfS0_S0_Pf:
	v_readfirstlane_b32 s29, v0
	v_cmp_gt_u32_e32 vcc, 32, v0
	s_nop 1
	s_and_saveexec_b64 s[30:31], vcc
	v_mov_b32_e32 v1, 0x10000
	v_lshl_or_b32 v1, v0, 2, v1
	v_mov_b32_e32 v2, 0
	ds_write_b32 v1, v2
	s_or_b64 exec, exec, s[30:31]
	s_load_dwordx4 s[4:7], s[0:1], 0x0
	s_load_dwordx4 s[8:11], s[0:1], 0x10
	s_lshr_b32 s12, s29, 6
	s_mov_b32 s51, 0x44800000
	s_mov_b32 s38, 0
	s_mov_b32 s39, -1
	s_mov_b32 s92, -1
	s_mov_b32 s93, 0xffff
	s_mov_b32 s94, 0xffff
	s_mov_b32 s95, 0xffff
	v_and_b32_e32 v8, 63, v0
	v_and_b32_e32 v169, 15, v0
	v_bfe_u32 v164, v0, 4, 2
	v_lshlrev_b32_e32 v167, 3, v164
	v_xor_b32_e32 v168, 16, v167
	v_sub_u32_e32 v165, v167, v169
	v_sub_u32_e32 v166, v168, v169
	v_add_u32_e32 v172, 0, v165
	v_med3_i32 v172, v172, 0, 10
	v_lshlrev_b32_e32 v172, 2, v172
	v_add_u32_e32 v173, 1, v165
	v_med3_i32 v173, v173, 0, 10
	v_lshlrev_b32_e32 v173, 2, v173
	v_add_u32_e32 v174, 2, v165
	v_med3_i32 v174, v174, 0, 10
	v_lshlrev_b32_e32 v174, 2, v174
	v_add_u32_e32 v175, 3, v165
	v_med3_i32 v175, v175, 0, 10
	v_lshlrev_b32_e32 v175, 2, v175
	v_add_u32_e32 v176, 4, v165
	v_med3_i32 v176, v176, 0, 10
	v_lshlrev_b32_e32 v176, 2, v176
	v_add_u32_e32 v177, 5, v165
	v_med3_i32 v177, v177, 0, 10
	v_lshlrev_b32_e32 v177, 2, v177
	v_add_u32_e32 v178, 6, v165
	v_med3_i32 v178, v178, 0, 10
	v_lshlrev_b32_e32 v178, 2, v178
	v_add_u32_e32 v179, 7, v165
	v_med3_i32 v179, v179, 0, 10
	v_lshlrev_b32_e32 v179, 2, v179
	v_add_u32_e32 v180, 0, v166
	v_med3_i32 v180, v180, 0, 10
	v_lshlrev_b32_e32 v180, 2, v180
	v_add_u32_e32 v181, 1, v166
	v_med3_i32 v181, v181, 0, 10
	v_lshlrev_b32_e32 v181, 2, v181
	v_add_u32_e32 v182, 2, v166
	v_med3_i32 v182, v182, 0, 10
	v_lshlrev_b32_e32 v182, 2, v182
	v_add_u32_e32 v183, 3, v166
	v_med3_i32 v183, v183, 0, 10
	v_lshlrev_b32_e32 v183, 2, v183
	v_add_u32_e32 v184, 4, v166
	v_med3_i32 v184, v184, 0, 10
	v_lshlrev_b32_e32 v184, 2, v184
	v_add_u32_e32 v185, 5, v166
	v_med3_i32 v185, v185, 0, 10
	v_lshlrev_b32_e32 v185, 2, v185
	v_add_u32_e32 v186, 6, v166
	v_med3_i32 v186, v186, 0, 10
	v_lshlrev_b32_e32 v186, 2, v186
	v_add_u32_e32 v187, 7, v166
	v_med3_i32 v187, v187, 0, 10
	v_lshlrev_b32_e32 v187, 2, v187
	s_waitcnt lgkmcnt(0)
	global_load_dword v188, v172, s[8:9]
	global_load_dword v189, v173, s[8:9]
	global_load_dword v190, v174, s[8:9]
	global_load_dword v191, v175, s[8:9]
	global_load_dword v192, v176, s[8:9]
	global_load_dword v193, v177, s[8:9]
	global_load_dword v194, v178, s[8:9]
	global_load_dword v195, v179, s[8:9]
	global_load_dword v196, v180, s[8:9]
	global_load_dword v197, v181, s[8:9]
	global_load_dword v198, v182, s[8:9]
	global_load_dword v199, v183, s[8:9]
	global_load_dword v200, v184, s[8:9]
	global_load_dword v201, v185, s[8:9]
	global_load_dword v202, v186, s[8:9]
	global_load_dword v203, v187, s[8:9]
	s_load_dwordx8 s[40:47], s[8:9], 0x0
	s_load_dwordx2 s[48:49], s[8:9], 0x20
	s_load_dword s50, s[8:9], 0x28
	s_and_b32 s13, s2, 7
	s_lshl_b32 s13, s13, 5
	s_lshr_b32 s14, s2, 3
	s_add_u32 s13, s13, s14
	s_lshr_b32 s14, s13, 3
	s_and_b32 s15, s13, 7
	s_lshl_b32 s16, s14, 20
	s_lshl_b32 s17, s15, 17
	s_add_u32 s16, s16, s17
	s_lshl_b32 s17, s12, 8
	s_add_u32 s16, s16, s17
	s_add_u32 s18, s4, s16
	s_addc_u32 s19, s5, 0
	s_add_u32 s20, s6, s16
	s_addc_u32 s21, s7, 0
	s_mov_b32 s52, s18
	s_mov_b32 s53, s19
	s_add_u32 s54, s18, 0x1000
	s_addc_u32 s55, s19, 0
	s_add_u32 s56, s18, 0x2000
	s_addc_u32 s57, s19, 0
	s_add_u32 s58, s18, 0x3000
	s_addc_u32 s59, s19, 0
	s_add_u32 s60, s18, 0x10000
	s_addc_u32 s61, s19, 0
	s_add_u32 s62, s18, 0x11000
	s_addc_u32 s63, s19, 0
	s_add_u32 s64, s18, 0x12000
	s_addc_u32 s65, s19, 0
	s_add_u32 s66, s18, 0x13000
	s_addc_u32 s67, s19, 0
	s_mov_b32 s68, s20
	s_mov_b32 s69, s21
	s_add_u32 s70, s20, 0x1000
	s_addc_u32 s71, s21, 0
	s_add_u32 s72, s20, 0x2000
	s_addc_u32 s73, s21, 0
	s_add_u32 s74, s20, 0x3000
	s_addc_u32 s75, s21, 0
	s_add_u32 s76, s20, 0x10000
	s_addc_u32 s77, s21, 0
	s_add_u32 s78, s20, 0x11000
	s_addc_u32 s79, s21, 0
	s_add_u32 s80, s20, 0x12000
	s_addc_u32 s81, s21, 0
	s_add_u32 s82, s20, 0x13000
	s_addc_u32 s83, s21, 0
	s_cmp_eq_u32 s15, 7
	s_cselect_b32 s22, 0, 0x20000
	s_add_u32 s84, s18, s22
	s_addc_u32 s85, s19, 0
	s_add_u32 s86, s18, s22
	s_addc_u32 s87, s19, 0
	s_add_u32 s86, s86, 0x1000
	s_addc_u32 s87, s87, 0
	s_add_u32 s88, s20, s22
	s_addc_u32 s89, s21, 0
	s_add_u32 s90, s20, s22
	s_addc_u32 s91, s21, 0
	s_add_u32 s90, s90, 0x1000
	s_addc_u32 s91, s91, 0
	v_lshrrev_b32_e32 v167, 2, v169
	v_lshlrev_b32_e32 v167, 5, v167
	v_and_b32_e32 v168, 1, v169
	v_lshl_or_b32 v167, v168, 4, v167
	v_bfe_u32 v168, v169, 1, 1
	v_lshl_or_b32 v167, v168, 7, v167
	v_lshl_or_b32 v9, v164, 14, v167
	v_and_b32_e32 v168, 1, v164
	v_lshl_or_b32 v23, v168, 14, v167
	v_lshrrev_b32_e32 v168, 1, v164
	v_lshl_or_b32 v23, v168, 13, v23
	global_load_dwordx4 v[36:39], v9, s[52:53] offset:0 nt
	global_load_dwordx4 v[40:43], v9, s[52:53] offset:2048 nt
	global_load_dwordx4 v[68:71], v9, s[68:69] offset:0 nt
	global_load_dwordx4 v[72:75], v9, s[68:69] offset:2048 nt
	global_load_dwordx4 v[44:47], v9, s[54:55] offset:0 nt
	global_load_dwordx4 v[48:51], v9, s[54:55] offset:2048 nt
	global_load_dwordx4 v[76:79], v9, s[70:71] offset:0 nt
	global_load_dwordx4 v[80:83], v9, s[70:71] offset:2048 nt
	global_load_dwordx4 v[52:55], v9, s[56:57] offset:0 nt
	global_load_dwordx4 v[56:59], v9, s[56:57] offset:2048 nt
	global_load_dwordx4 v[84:87], v9, s[72:73] offset:0 nt
	global_load_dwordx4 v[88:91], v9, s[72:73] offset:2048 nt
	global_load_dwordx4 v[60:63], v9, s[58:59] offset:0 nt
	global_load_dwordx4 v[64:67], v9, s[58:59] offset:2048 nt
	global_load_dwordx4 v[92:95], v9, s[74:75] offset:0 nt
	global_load_dwordx4 v[96:99], v9, s[74:75] offset:2048 nt
	global_load_dwordx4 v[100:103], v9, s[60:61] offset:0 nt
	global_load_dwordx4 v[104:107], v9, s[60:61] offset:2048 nt
	global_load_dwordx4 v[132:135], v9, s[76:77] offset:0 nt
	global_load_dwordx4 v[136:139], v9, s[76:77] offset:2048 nt
	global_load_dwordx4 v[108:111], v9, s[62:63] offset:0 nt
	global_load_dwordx4 v[112:115], v9, s[62:63] offset:2048 nt
	global_load_dwordx4 v[140:143], v9, s[78:79] offset:0 nt
	global_load_dwordx4 v[144:147], v9, s[78:79] offset:2048 nt
	global_load_dwordx4 v[116:119], v9, s[64:65] offset:0 nt
	global_load_dwordx4 v[120:123], v9, s[64:65] offset:2048 nt
	global_load_dwordx4 v[148:151], v9, s[80:81] offset:0 nt
	global_load_dwordx4 v[152:155], v9, s[80:81] offset:2048 nt
	global_load_dwordx4 v[124:127], v9, s[66:67] offset:0 nt
	global_load_dwordx4 v[128:131], v9, s[66:67] offset:2048 nt
	global_load_dwordx4 v[156:159], v9, s[82:83] offset:0 nt
	global_load_dwordx4 v[160:163], v9, s[82:83] offset:2048 nt
	s_waitcnt lgkmcnt(0)
	v_mov_b32_e32 v229, 0x44800000
	v_fma_mixlo_f16 v228, s40, v229, 0
	v_cvt_f32_f16_e32 v228, v228
	v_cvt_f64_f32_e32 v[212:213], v228
	v_add_f64 v[212:213], v[212:213], 0
	v_fma_mixlo_f16 v228, s41, v229, 0
	v_cvt_f32_f16_e32 v228, v228
	v_cvt_f64_f32_e32 v[214:215], v228
	v_add_f64 v[212:213], v[212:213], v[214:215]
	v_fma_mixlo_f16 v228, s42, v229, 0
	v_cvt_f32_f16_e32 v228, v228
	v_cvt_f64_f32_e32 v[214:215], v228
	v_add_f64 v[212:213], v[212:213], v[214:215]
	v_fma_mixlo_f16 v228, s43, v229, 0
	v_cvt_f32_f16_e32 v228, v228
	v_cvt_f64_f32_e32 v[214:215], v228
	v_add_f64 v[212:213], v[212:213], v[214:215]
	v_fma_mixlo_f16 v228, s44, v229, 0
	v_cvt_f32_f16_e32 v228, v228
	v_cvt_f64_f32_e32 v[214:215], v228
	v_add_f64 v[212:213], v[212:213], v[214:215]
	v_fma_mixlo_f16 v228, s45, v229, 0
	v_cvt_f32_f16_e32 v228, v228
	v_cvt_f64_f32_e32 v[214:215], v228
	v_add_f64 v[212:213], v[212:213], v[214:215]
	v_fma_mixlo_f16 v228, s46, v229, 0
	v_cvt_f32_f16_e32 v228, v228
	v_cvt_f64_f32_e32 v[214:215], v228
	v_add_f64 v[212:213], v[212:213], v[214:215]
	v_fma_mixlo_f16 v228, s47, v229, 0
	v_cvt_f32_f16_e32 v228, v228
	v_cvt_f64_f32_e32 v[214:215], v228
	v_add_f64 v[212:213], v[212:213], v[214:215]
	v_fma_mixlo_f16 v228, s48, v229, 0
	v_cvt_f32_f16_e32 v228, v228
	v_cvt_f64_f32_e32 v[214:215], v228
	v_add_f64 v[212:213], v[212:213], v[214:215]
	v_fma_mixlo_f16 v228, s49, v229, 0
	v_cvt_f32_f16_e32 v228, v228
	v_cvt_f64_f32_e32 v[214:215], v228
	v_add_f64 v[212:213], v[212:213], v[214:215]
	v_fma_mixlo_f16 v228, s50, v229, 0
	v_cvt_f32_f16_e32 v228, v228
	v_cvt_f64_f32_e32 v[214:215], v228
	v_add_f64 v[212:213], v[212:213], v[214:215]
	v_mul_f64 v[212:213], v[212:213], v[212:213]
	v_mul_f64 v[216:217], v[212:213], 0.5
	v_add_f64 v[218:219], v[216:217], v[216:217]
	s_mov_b32 s36, 0xeb1c432d
	s_mov_b32 s37, 0x3f1a36e2
	v_mul_f64 v[220:221], v[212:213], s[36:37]
	v_mul_f64 v[222:223], v[216:217], v[218:219]
	v_fmac_f64_e32 v[222:223], v[212:213], v[220:221]
	v_add_f64 v[224:225], v[212:213], v[212:213]
	s_mov_b32 s36, 0x487fcb92
	s_mov_b32 s37, 0x3f4d7dbf
	v_mul_f64 v[226:227], v[212:213], s[36:37]
	v_cvt_f32_f64_e32 v0, v[226:227]
	v_mov_b32_e32 v1, v0
	v_mov_b32_e32 v2, v0
	v_mov_b32_e32 v3, v0
	v_cvt_f32_f64_e32 v10, v[218:219]
	v_cvt_f32_f64_e32 v11, v[222:223]
	v_cvt_f32_f64_e32 v12, v[212:213]
	v_cvt_f32_f64_e32 v13, v[224:225]
	v_mul_f64 v[226:227], v[212:213], v[226:227]
	v_cvt_f32_f64_e32 v14, v[226:227]
	v_lshlrev_b32_e32 v167, 2, v164
	s_cmp_eq_u32 s12, 0
	s_cselect_b32 s23, 6, 64
	v_add_u32_e32 v168, 0, v167
	v_cmp_gt_u32_e32 vcc, s23, v168
	s_nop 1
	v_cndmask_b32_e64 v15, 0, 1.0, vcc
	v_add_u32_e32 v168, 1, v167
	v_cmp_gt_u32_e32 vcc, s23, v168
	s_nop 1
	v_cndmask_b32_e64 v16, 0, 1.0, vcc
	v_add_u32_e32 v168, 2, v167
	v_cmp_gt_u32_e32 vcc, s23, v168
	s_nop 1
	v_cndmask_b32_e64 v17, 0, 1.0, vcc
	v_add_u32_e32 v168, 3, v167
	v_cmp_gt_u32_e32 vcc, s23, v168
	s_nop 1
	v_cndmask_b32_e64 v18, 0, 1.0, vcc
	v_and_b32_e32 v167, 31, v8
	v_lshlrev_b32_e32 v167, 4, v167
	s_lshl_b32 s24, s12, 11
	s_add_i32 s25, s12, 7
	s_and_b32 s25, s25, 7
	s_lshl_b32 s26, s25, 11
	v_or_b32_e32 v4, s24, v167
	v_or_b32_e32 v5, s26, v167
	s_lshl_b32 s27, s12, 2
	s_add_u32 s27, s27, 0x10000
	s_lshl_b32 s28, s25, 2
	s_add_u32 s28, s28, 0x10000
	v_mov_b32_e32 v6, s27
	v_mov_b32_e32 v7, s28
	v_mov_b32_e32 v19, 0
	v_mov_b32_e32 v20, 0
	v_mov_b32_e32 v21, 0
	v_mov_b32_e32 v22, 0
	s_waitcnt vmcnt(32)
	v_cmp_lt_u32_e64 s[32:33], 31, v8
	v_cmp_gt_u32_e64 s[34:35], 32, v8
	v_fma_mixlo_f16 v204, v188, s51, 0
	v_add_u32_e32 v167, 0, v165
	v_cmp_gt_u32_e32 vcc, 11, v167
	s_nop 1
	v_cndmask_b32_e32 v204, 0, v204, vcc
	v_fma_mixlo_f16 v205, v189, s51, 0
	v_add_u32_e32 v167, 1, v165
	v_cmp_gt_u32_e32 vcc, 11, v167
	s_nop 1
	v_cndmask_b32_e32 v205, 0, v205, vcc
	v_fma_mixlo_f16 v206, v190, s51, 0
	v_add_u32_e32 v167, 2, v165
	v_cmp_gt_u32_e32 vcc, 11, v167
	s_nop 1
	v_cndmask_b32_e32 v206, 0, v206, vcc
	v_fma_mixlo_f16 v207, v191, s51, 0
	v_add_u32_e32 v167, 3, v165
	v_cmp_gt_u32_e32 vcc, 11, v167
	s_nop 1
	v_cndmask_b32_e32 v207, 0, v207, vcc
	v_fma_mixlo_f16 v208, v192, s51, 0
	v_add_u32_e32 v167, 4, v165
	v_cmp_gt_u32_e32 vcc, 11, v167
	s_nop 1
	v_cndmask_b32_e32 v208, 0, v208, vcc
	v_fma_mixlo_f16 v209, v193, s51, 0
	v_add_u32_e32 v167, 5, v165
	v_cmp_gt_u32_e32 vcc, 11, v167
	s_nop 1
	v_cndmask_b32_e32 v209, 0, v209, vcc
	v_fma_mixlo_f16 v210, v194, s51, 0
	v_add_u32_e32 v167, 6, v165
	v_cmp_gt_u32_e32 vcc, 11, v167
	s_nop 1
	v_cndmask_b32_e32 v210, 0, v210, vcc
	v_fma_mixlo_f16 v211, v195, s51, 0
	v_add_u32_e32 v167, 7, v165
	v_cmp_gt_u32_e32 vcc, 11, v167
	s_nop 1
	v_cndmask_b32_e32 v211, 0, v211, vcc
	v_pack_b32_f16 v24, v204, v205
	v_pack_b32_f16 v25, v206, v207
	v_pack_b32_f16 v26, v208, v209
	v_pack_b32_f16 v27, v210, v211
	v_fma_mixlo_f16 v204, v196, s51, 0
	v_add_u32_e32 v167, 0, v166
	v_cmp_gt_u32_e32 vcc, 11, v167
	s_nop 1
	v_cndmask_b32_e32 v204, 0, v204, vcc
	v_fma_mixlo_f16 v205, v197, s51, 0
	v_add_u32_e32 v167, 1, v166
	v_cmp_gt_u32_e32 vcc, 11, v167
	s_nop 1
	v_cndmask_b32_e32 v205, 0, v205, vcc
	v_fma_mixlo_f16 v206, v198, s51, 0
	v_add_u32_e32 v167, 2, v166
	v_cmp_gt_u32_e32 vcc, 11, v167
	s_nop 1
	v_cndmask_b32_e32 v206, 0, v206, vcc
	v_fma_mixlo_f16 v207, v199, s51, 0
	v_add_u32_e32 v167, 3, v166
	v_cmp_gt_u32_e32 vcc, 11, v167
	s_nop 1
	v_cndmask_b32_e32 v207, 0, v207, vcc
	v_fma_mixlo_f16 v208, v200, s51, 0
	v_add_u32_e32 v167, 4, v166
	v_cmp_gt_u32_e32 vcc, 11, v167
	s_nop 1
	v_cndmask_b32_e32 v208, 0, v208, vcc
	v_fma_mixlo_f16 v209, v201, s51, 0
	v_add_u32_e32 v167, 5, v166
	v_cmp_gt_u32_e32 vcc, 11, v167
	s_nop 1
	v_cndmask_b32_e32 v209, 0, v209, vcc
	v_fma_mixlo_f16 v210, v202, s51, 0
	v_add_u32_e32 v167, 6, v166
	v_cmp_gt_u32_e32 vcc, 11, v167
	s_nop 1
	v_cndmask_b32_e32 v210, 0, v210, vcc
	v_fma_mixlo_f16 v211, v203, s51, 0
	v_add_u32_e32 v167, 7, v166
	v_cmp_gt_u32_e32 vcc, 11, v167
	s_nop 1
	v_cndmask_b32_e32 v211, 0, v211, vcc
	v_pack_b32_f16 v167, v204, v205
	v_cndmask_b32_e64 v28, 0, v167, s[32:33]
	v_cndmask_b32_e64 v32, 0, v167, s[34:35]
	v_pack_b32_f16 v167, v206, v207
	v_cndmask_b32_e64 v29, 0, v167, s[32:33]
	v_cndmask_b32_e64 v33, 0, v167, s[34:35]
	v_pack_b32_f16 v167, v208, v209
	v_cndmask_b32_e64 v30, 0, v167, s[32:33]
	v_cndmask_b32_e64 v34, 0, v167, s[34:35]
	v_pack_b32_f16 v167, v210, v211
	v_cndmask_b32_e64 v31, 0, v167, s[32:33]
	v_cndmask_b32_e64 v35, 0, v167, s[34:35]
	s_waitcnt lgkmcnt(0)
	s_barrier
	s_waitcnt vmcnt(28)
	v_cvt_pk_f16_f32 v164, v36, v40
	v_cvt_pk_f16_f32 v180, v68, v72
	v_pk_add_f16 v164, v164, -0.5 op_sel_hi:[1,0]
	v_pk_add_f16 v180, v180, -0.5 op_sel_hi:[1,0]
	v_pk_mul_f16 v196, v180, v180
	v_pk_mul_f16 v212, v164, v180
	v_pk_fma_f16 v196, v164, v164, v196
	v_cvt_pk_f16_f32 v168, v37, v41
	v_cvt_pk_f16_f32 v184, v69, v73
	v_pk_add_f16 v168, v168, -0.5 op_sel_hi:[1,0]
	v_pk_add_f16 v184, v184, -0.5 op_sel_hi:[1,0]
	v_pk_mul_f16 v200, v184, v184
	v_pk_mul_f16 v216, v168, v184
	v_pk_fma_f16 v200, v168, v168, v200
	v_cvt_pk_f16_f32 v172, v38, v42
	v_cvt_pk_f16_f32 v188, v70, v74
	v_pk_add_f16 v172, v172, -0.5 op_sel_hi:[1,0]
	v_pk_add_f16 v188, v188, -0.5 op_sel_hi:[1,0]
	v_pk_mul_f16 v204, v188, v188
	v_pk_mul_f16 v220, v172, v188
	v_pk_fma_f16 v204, v172, v172, v204
	v_cvt_pk_f16_f32 v176, v39, v43
	v_cvt_pk_f16_f32 v192, v71, v75
	v_pk_add_f16 v176, v176, -0.5 op_sel_hi:[1,0]
	v_pk_add_f16 v192, v192, -0.5 op_sel_hi:[1,0]
	v_pk_mul_f16 v208, v192, v192
	v_pk_mul_f16 v224, v176, v192
	v_pk_fma_f16 v208, v176, v176, v208
	s_waitcnt vmcnt(24)
	v_cvt_pk_f16_f32 v165, v44, v48
	v_cvt_pk_f16_f32 v181, v76, v80
	v_pk_add_f16 v165, v165, -0.5 op_sel_hi:[1,0]
	v_pk_add_f16 v181, v181, -0.5 op_sel_hi:[1,0]
	v_pk_mul_f16 v197, v181, v181
	v_pk_mul_f16 v213, v165, v181
	v_pk_fma_f16 v197, v165, v165, v197
	v_cvt_pk_f16_f32 v169, v45, v49
	v_cvt_pk_f16_f32 v185, v77, v81
	v_pk_add_f16 v169, v169, -0.5 op_sel_hi:[1,0]
	v_pk_add_f16 v185, v185, -0.5 op_sel_hi:[1,0]
	v_pk_mul_f16 v201, v185, v185
	v_pk_mul_f16 v217, v169, v185
	v_pk_fma_f16 v201, v169, v169, v201
	v_cvt_pk_f16_f32 v173, v46, v50
	v_cvt_pk_f16_f32 v189, v78, v82
	v_pk_add_f16 v173, v173, -0.5 op_sel_hi:[1,0]
	v_pk_add_f16 v189, v189, -0.5 op_sel_hi:[1,0]
	v_pk_mul_f16 v205, v189, v189
	v_pk_mul_f16 v221, v173, v189
	v_pk_fma_f16 v205, v173, v173, v205
	v_cvt_pk_f16_f32 v177, v47, v51
	v_cvt_pk_f16_f32 v193, v79, v83
	v_pk_add_f16 v177, v177, -0.5 op_sel_hi:[1,0]
	v_pk_add_f16 v193, v193, -0.5 op_sel_hi:[1,0]
	v_pk_mul_f16 v209, v193, v193
	v_pk_mul_f16 v225, v177, v193
	v_pk_fma_f16 v209, v177, v177, v209
	s_waitcnt vmcnt(20)
	v_cvt_pk_f16_f32 v166, v52, v56
	v_cvt_pk_f16_f32 v182, v84, v88
	v_pk_add_f16 v166, v166, -0.5 op_sel_hi:[1,0]
	v_pk_add_f16 v182, v182, -0.5 op_sel_hi:[1,0]
	v_pk_mul_f16 v198, v182, v182
	v_pk_mul_f16 v214, v166, v182
	v_pk_fma_f16 v198, v166, v166, v198
	v_cvt_pk_f16_f32 v170, v53, v57
	v_cvt_pk_f16_f32 v186, v85, v89
	v_pk_add_f16 v170, v170, -0.5 op_sel_hi:[1,0]
	v_pk_add_f16 v186, v186, -0.5 op_sel_hi:[1,0]
	v_pk_mul_f16 v202, v186, v186
	v_pk_mul_f16 v218, v170, v186
	v_pk_fma_f16 v202, v170, v170, v202
	v_cvt_pk_f16_f32 v174, v54, v58
	v_cvt_pk_f16_f32 v190, v86, v90
	v_pk_add_f16 v174, v174, -0.5 op_sel_hi:[1,0]
	v_pk_add_f16 v190, v190, -0.5 op_sel_hi:[1,0]
	v_pk_mul_f16 v206, v190, v190
	v_pk_mul_f16 v222, v174, v190
	v_pk_fma_f16 v206, v174, v174, v206
	v_cvt_pk_f16_f32 v178, v55, v59
	v_cvt_pk_f16_f32 v194, v87, v91
	v_pk_add_f16 v178, v178, -0.5 op_sel_hi:[1,0]
	v_pk_add_f16 v194, v194, -0.5 op_sel_hi:[1,0]
	v_pk_mul_f16 v210, v194, v194
	v_pk_mul_f16 v226, v178, v194
	v_pk_fma_f16 v210, v178, v178, v210
	s_waitcnt vmcnt(16)
	v_cvt_pk_f16_f32 v167, v60, v64
	v_cvt_pk_f16_f32 v183, v92, v96
	v_pk_add_f16 v167, v167, -0.5 op_sel_hi:[1,0]
	v_pk_add_f16 v183, v183, -0.5 op_sel_hi:[1,0]
	v_pk_mul_f16 v199, v183, v183
	v_pk_mul_f16 v215, v167, v183
	v_pk_fma_f16 v199, v167, v167, v199
	v_cvt_pk_f16_f32 v171, v61, v65
	v_cvt_pk_f16_f32 v187, v93, v97
	v_pk_add_f16 v171, v171, -0.5 op_sel_hi:[1,0]
	v_pk_add_f16 v187, v187, -0.5 op_sel_hi:[1,0]
	v_pk_mul_f16 v203, v187, v187
	v_pk_mul_f16 v219, v171, v187
	v_pk_fma_f16 v203, v171, v171, v203
	v_cvt_pk_f16_f32 v175, v62, v66
	v_cvt_pk_f16_f32 v191, v94, v98
	v_pk_add_f16 v175, v175, -0.5 op_sel_hi:[1,0]
	v_pk_add_f16 v191, v191, -0.5 op_sel_hi:[1,0]
	v_pk_mul_f16 v207, v191, v191
	v_pk_mul_f16 v223, v175, v191
	v_pk_fma_f16 v207, v175, v175, v207
	v_cvt_pk_f16_f32 v179, v63, v67
	v_cvt_pk_f16_f32 v195, v95, v99
	v_pk_add_f16 v179, v179, -0.5 op_sel_hi:[1,0]
	v_pk_add_f16 v195, v195, -0.5 op_sel_hi:[1,0]
	v_pk_mul_f16 v211, v195, v195
	v_pk_mul_f16 v227, v179, v195
	v_pk_fma_f16 v211, v179, v179, v211
	v_mfma_f32_16x16x32_f16 v[68:71], v[164:167], v[24:27], 0
	v_mfma_f32_16x16x32_f16 v[72:75], v[168:171], v[24:27], 0
	v_mfma_f32_16x16x32_f16 v[76:79], v[172:175], v[24:27], 0
	v_mfma_f32_16x16x32_f16 v[80:83], v[176:179], v[24:27], 0
	v_mfma_f32_16x16x32_f16 v[84:87], v[180:183], v[24:27], 0
	v_mfma_f32_16x16x32_f16 v[88:91], v[184:187], v[24:27], 0
	v_mfma_f32_16x16x32_f16 v[92:95], v[188:191], v[24:27], 0
	v_mfma_f32_16x16x32_f16 v[96:99], v[192:195], v[24:27], 0
	s_nop 1
	v_cvt_pk_f16_f32 v36, v68, v72
	s_nop 0
	v_cvt_pk_f16_f32 v37, v76, v80
	v_cvt_pk_f16_f32 v38, v69, v73
	v_cvt_pk_f16_f32 v39, v77, v81
	v_cvt_pk_f16_f32 v40, v70, v74
	v_cvt_pk_f16_f32 v41, v78, v82
	v_cvt_pk_f16_f32 v42, v71, v75
	v_cvt_pk_f16_f32 v43, v79, v83
	v_mfma_f32_16x16x32_f16 v[68:71], v[196:199], v[24:27], 0
	v_mfma_f32_16x16x32_f16 v[72:75], v[200:203], v[24:27], 0
	v_mfma_f32_16x16x32_f16 v[76:79], v[204:207], v[24:27], 0
	v_mfma_f32_16x16x32_f16 v[80:83], v[208:211], v[24:27], 0
	v_cvt_pk_f16_f32 v44, v84, v88
	v_cvt_pk_f16_f32 v45, v92, v96
	v_cvt_pk_f16_f32 v46, v85, v89
	v_cvt_pk_f16_f32 v47, v93, v97
	v_cvt_pk_f16_f32 v48, v86, v90
	v_cvt_pk_f16_f32 v49, v94, v98
	v_cvt_pk_f16_f32 v50, v87, v91
	v_cvt_pk_f16_f32 v51, v95, v99
	v_mfma_f32_16x16x32_f16 v[84:87], v[212:215], v[24:27], 0
	v_mfma_f32_16x16x32_f16 v[88:91], v[216:219], v[24:27], 0
	v_mfma_f32_16x16x32_f16 v[92:95], v[220:223], v[24:27], 0
	v_mfma_f32_16x16x32_f16 v[96:99], v[224:227], v[24:27], 0
	v_cvt_pk_f16_f32 v52, v68, v72
	v_cvt_pk_f16_f32 v53, v76, v80
	v_cvt_pk_f16_f32 v54, v69, v73
	v_cvt_pk_f16_f32 v55, v77, v81
	v_cvt_pk_f16_f32 v56, v70, v74
	v_cvt_pk_f16_f32 v57, v78, v82
	v_cvt_pk_f16_f32 v58, v71, v75
	v_cvt_pk_f16_f32 v59, v79, v83
	v_cvt_pk_f16_f32 v60, v84, v88
	v_cvt_pk_f16_f32 v61, v92, v96
	v_cvt_pk_f16_f32 v62, v85, v89
	v_cvt_pk_f16_f32 v63, v93, v97
	v_cvt_pk_f16_f32 v64, v86, v90
	v_cvt_pk_f16_f32 v65, v94, v98
	v_cvt_pk_f16_f32 v66, v87, v91
	v_cvt_pk_f16_f32 v67, v95, v99
	s_mov_b64 exec, s[38:39]
	ds_write_b128 v4, v[40:43] offset:0
	ds_write_b128 v4, v[48:51] offset:512
	ds_write_b128 v4, v[56:59] offset:1024
	ds_write_b128 v4, v[64:67] offset:1536
	s_mov_b64 exec, -1
	v_mfma_f32_16x16x32_f16 v[68:71], v[24:27], v[36:39], 0
	v_mfma_f32_16x16x32_f16 v[72:75], v[24:27], v[44:47], 0
	v_mfma_f32_16x16x32_f16 v[76:79], v[24:27], v[52:55], v[0:3]
	v_mfma_f32_16x16x32_f16 v[80:83], v[24:27], v[60:63], 0
	v_mfma_f32_16x16x32_f16 v[84:87], v[28:31], v[36:39], 0
	v_mfma_f32_16x16x32_f16 v[88:91], v[28:31], v[44:47], 0
	v_mfma_f32_16x16x32_f16 v[92:95], v[28:31], v[52:55], v[0:3]
	v_mfma_f32_16x16x32_f16 v[96:99], v[28:31], v[60:63], 0
	v_mfma_f32_16x16x32_f16 v[84:87], v[32:35], v[40:43], v[84:87]
	v_mfma_f32_16x16x32_f16 v[88:91], v[32:35], v[48:51], v[88:91]
	v_mfma_f32_16x16x32_f16 v[92:95], v[32:35], v[56:59], v[92:95]
	v_mfma_f32_16x16x32_f16 v[96:99], v[32:35], v[64:67], v[96:99]
	s_waitcnt lgkmcnt(0)
	ds_write_b32 v6, v6 offset:0
	ds_read_b32 v9, v7 offset:0
	v_mul_f32_e32 v244, v68, v72
	v_mul_f32_e32 v250, v69, v73
	v_mul_f32_e64 v245, -v72, v72
	v_mul_f32_e64 v251, -v73, v73
	v_add_f32_e32 v246, v68, v72
	v_add_f32_e32 v252, v69, v73
	v_fma_f32 v245, -v68, v68, v245
	v_fma_f32 v251, -v69, v69, v251
	v_fma_f32 v247, v10, v246, v11
	v_fma_f32 v253, v10, v252, v11
	v_fma_f32 v246, v13, v80, v14
	v_fma_f32 v252, v13, v81, v14
	v_fma_f32 v248, v12, v76, v245
	v_fma_f32 v254, v12, v77, v251
	v_fma_f32 v249, 2.0, v244, v247
	v_fma_f32 v255, 2.0, v250, v253
	v_sub_f32_e32 v247, v247, v245
	v_sub_f32_e32 v253, v253, v251
	v_fma_f32 v246, -2.0, v244, v246
	v_fma_f32 v252, -2.0, v250, v252
	v_mul_f32_e32 v247, v247, v248
	v_mul_f32_e32 v253, v253, v254
	v_rcp_f32_e32 v247, v247
	v_rcp_f32_e32 v253, v253
	v_mul_f32_e32 v249, v249, v246
	v_mul_f32_e32 v255, v255, v252
	v_fma_f32 v19, v249, v247, v19
	v_fma_f32 v19, v255, v253, v19
	v_mul_f32_e32 v244, v70, v74
	v_mul_f32_e32 v250, v71, v75
	v_mul_f32_e64 v245, -v74, v74
	v_mul_f32_e64 v251, -v75, v75
	v_add_f32_e32 v246, v70, v74
	v_add_f32_e32 v252, v71, v75
	v_fma_f32 v245, -v70, v70, v245
	v_fma_f32 v251, -v71, v71, v251
	v_fma_f32 v247, v10, v246, v11
	v_fma_f32 v253, v10, v252, v11
	v_fma_f32 v246, v13, v82, v14
	v_fma_f32 v252, v13, v83, v14
	v_fma_f32 v248, v12, v78, v245
	v_fma_f32 v254, v12, v79, v251
	v_fma_f32 v249, 2.0, v244, v247
	v_fma_f32 v255, 2.0, v250, v253
	v_sub_f32_e32 v247, v247, v245
	v_sub_f32_e32 v253, v253, v251
	v_fma_f32 v246, -2.0, v244, v246
	v_fma_f32 v252, -2.0, v250, v252
	v_mul_f32_e32 v247, v247, v248
	v_mul_f32_e32 v253, v253, v254
	v_rcp_f32_e32 v247, v247
	v_rcp_f32_e32 v253, v253
	v_mul_f32_e32 v249, v249, v246
	v_mul_f32_e32 v255, v255, v252
	v_fma_f32 v20, v249, v247, v20
	v_fma_f32 v20, v255, v253, v20
	v_mfma_f32_16x16x32_f16 v[68:71], v[24:27], v[40:43], 0
	v_mfma_f32_16x16x32_f16 v[72:75], v[24:27], v[48:51], 0
	v_mfma_f32_16x16x32_f16 v[76:79], v[24:27], v[56:59], v[0:3]
	v_mfma_f32_16x16x32_f16 v[80:83], v[24:27], v[64:67], 0
	s_waitcnt lgkmcnt(0)
	v_cmp_ne_u32_e32 vcc, 0, v9
	s_cbranch_vccnz .Lq_go_0

.Lq_go_0:
	ds_read_b128 v[228:231], v5 offset:0
	ds_read_b128 v[232:235], v5 offset:512
	ds_read_b128 v[236:239], v5 offset:1024
	ds_read_b128 v[240:243], v5 offset:1536
	v_mul_f32_e32 v244, v84, v88
	v_mul_f32_e32 v250, v85, v89
	v_mul_f32_e64 v245, -v88, v88
	v_mul_f32_e64 v251, -v89, v89
	v_add_f32_e32 v246, v84, v88
	v_add_f32_e32 v252, v85, v89
	v_fma_f32 v245, -v84, v84, v245
	v_fma_f32 v251, -v85, v85, v251
	v_fma_f32 v247, v10, v246, v11
	v_fma_f32 v253, v10, v252, v11
	v_fma_f32 v246, v13, v96, v14
	v_fma_f32 v252, v13, v97, v14
	v_fma_f32 v248, v12, v92, v245
	v_fma_f32 v254, v12, v93, v251
	v_fma_f32 v249, 2.0, v244, v247
	v_fma_f32 v255, 2.0, v250, v253
	v_sub_f32_e32 v247, v247, v245
	v_sub_f32_e32 v253, v253, v251
	v_fma_f32 v246, -2.0, v244, v246
	v_fma_f32 v252, -2.0, v250, v252
	v_mul_f32_e32 v247, v247, v248
	v_mul_f32_e32 v253, v253, v254
	v_rcp_f32_e32 v247, v247
	v_rcp_f32_e32 v253, v253
	v_mul_f32_e32 v249, v249, v246
	v_mul_f32_e32 v255, v255, v252
	v_fma_f32 v19, v249, v247, v19
	v_fma_f32 v19, v255, v253, v19
	v_mul_f32_e32 v244, v86, v90
	v_mul_f32_e32 v250, v87, v91
	v_mul_f32_e64 v245, -v90, v90
	v_mul_f32_e64 v251, -v91, v91
	v_add_f32_e32 v246, v86, v90
	v_add_f32_e32 v252, v87, v91
	v_fma_f32 v245, -v86, v86, v245
	v_fma_f32 v251, -v87, v87, v251
	v_fma_f32 v247, v10, v246, v11
	v_fma_f32 v253, v10, v252, v11
	v_fma_f32 v246, v13, v98, v14
	v_fma_f32 v252, v13, v99, v14
	v_fma_f32 v248, v12, v94, v245
	v_fma_f32 v254, v12, v95, v251
	v_fma_f32 v249, 2.0, v244, v247
	v_fma_f32 v255, 2.0, v250, v253
	v_sub_f32_e32 v247, v247, v245
	v_sub_f32_e32 v253, v253, v251
	v_fma_f32 v246, -2.0, v244, v246
	v_fma_f32 v252, -2.0, v250, v252
	v_mul_f32_e32 v247, v247, v248
	v_mul_f32_e32 v253, v253, v254
	v_rcp_f32_e32 v247, v247
	v_rcp_f32_e32 v253, v253
	v_mul_f32_e32 v249, v249, v246
	v_mul_f32_e32 v255, v255, v252
	v_fma_f32 v20, v249, v247, v20
	v_fma_f32 v20, v255, v253, v20
	s_waitcnt lgkmcnt(0)
	v_mfma_f32_16x16x32_f16 v[84:87], v[28:31], v[228:231], 0
	v_mfma_f32_16x16x32_f16 v[88:91], v[28:31], v[232:235], 0
	v_mfma_f32_16x16x32_f16 v[92:95], v[28:31], v[236:239], v[0:3]
	v_mfma_f32_16x16x32_f16 v[96:99], v[28:31], v[240:243], 0
	v_mfma_f32_16x16x32_f16 v[84:87], v[32:35], v[36:39], v[84:87]
	v_mfma_f32_16x16x32_f16 v[88:91], v[32:35], v[44:47], v[88:91]
	v_mfma_f32_16x16x32_f16 v[92:95], v[32:35], v[52:55], v[92:95]
	v_mfma_f32_16x16x32_f16 v[96:99], v[32:35], v[60:63], v[96:99]
	v_mul_f32_e32 v244, v68, v72
	v_mul_f32_e32 v250, v69, v73
	v_mul_f32_e64 v245, -v72, v72
	v_mul_f32_e64 v251, -v73, v73
	v_add_f32_e32 v246, v68, v72
	v_add_f32_e32 v252, v69, v73
	v_fma_f32 v245, -v68, v68, v245
	v_fma_f32 v251, -v69, v69, v251
	v_fma_f32 v247, v10, v246, v11
	v_fma_f32 v253, v10, v252, v11
	v_fma_f32 v246, v13, v80, v14
	v_fma_f32 v252, v13, v81, v14
	v_fma_f32 v248, v12, v76, v245
	v_fma_f32 v254, v12, v77, v251
	v_fma_f32 v249, 2.0, v244, v247
	v_fma_f32 v255, 2.0, v250, v253
	v_sub_f32_e32 v247, v247, v245
	v_sub_f32_e32 v253, v253, v251
	v_fma_f32 v246, -2.0, v244, v246
	v_fma_f32 v252, -2.0, v250, v252
	v_mul_f32_e32 v247, v247, v248
	v_mul_f32_e32 v253, v253, v254
	v_rcp_f32_e32 v247, v247
	v_rcp_f32_e32 v253, v253
	v_mul_f32_e32 v249, v249, v246
	v_mul_f32_e32 v255, v255, v252
	v_fma_f32 v19, v249, v247, v19
	v_fma_f32 v19, v255, v253, v19
	v_mul_f32_e32 v244, v70, v74
	v_mul_f32_e32 v250, v71, v75
	v_mul_f32_e64 v245, -v74, v74
	v_mul_f32_e64 v251, -v75, v75
	v_add_f32_e32 v246, v70, v74
	v_add_f32_e32 v252, v71, v75
	v_fma_f32 v245, -v70, v70, v245
	v_fma_f32 v251, -v71, v71, v251
	v_fma_f32 v247, v10, v246, v11
	v_fma_f32 v253, v10, v252, v11
	v_fma_f32 v246, v13, v82, v14
	v_fma_f32 v252, v13, v83, v14
	v_fma_f32 v248, v12, v78, v245
	v_fma_f32 v254, v12, v79, v251
	v_fma_f32 v249, 2.0, v244, v247
	v_fma_f32 v255, 2.0, v250, v253
	v_sub_f32_e32 v247, v247, v245
	v_sub_f32_e32 v253, v253, v251
	v_fma_f32 v246, -2.0, v244, v246
	v_fma_f32 v252, -2.0, v250, v252
	v_mul_f32_e32 v247, v247, v248
	v_mul_f32_e32 v253, v253, v254
	v_rcp_f32_e32 v247, v247
	v_rcp_f32_e32 v253, v253
	v_mul_f32_e32 v249, v249, v246
	v_mul_f32_e32 v255, v255, v252
	v_fma_f32 v20, v249, v247, v20
	v_fma_f32 v20, v255, v253, v20
	v_mul_f32_e32 v244, v84, v88
	v_mul_f32_e32 v250, v85, v89
	v_mul_f32_e64 v245, -v88, v88
	v_mul_f32_e64 v251, -v89, v89
	v_add_f32_e32 v246, v84, v88
	v_add_f32_e32 v252, v85, v89
	v_fma_f32 v245, -v84, v84, v245
	v_fma_f32 v251, -v85, v85, v251
	v_fma_f32 v247, v10, v246, v11
	v_fma_f32 v253, v10, v252, v11
	v_fma_f32 v246, v13, v96, v14
	v_fma_f32 v252, v13, v97, v14
	v_fma_f32 v248, v12, v92, v245
	v_fma_f32 v254, v12, v93, v251
	v_fma_f32 v249, 2.0, v244, v247
	v_fma_f32 v255, 2.0, v250, v253
	v_sub_f32_e32 v247, v247, v245
	v_sub_f32_e32 v253, v253, v251
	v_fma_f32 v246, -2.0, v244, v246
	v_fma_f32 v252, -2.0, v250, v252
	v_mul_f32_e32 v247, v247, v248
	v_mul_f32_e32 v253, v253, v254
	v_rcp_f32_e32 v247, v247
	v_rcp_f32_e32 v253, v253
	v_mul_f32_e32 v249, v249, v246
	v_mul_f32_e32 v255, v255, v252
	v_mul_f32_e32 v249, v249, v247
	v_mul_f32_e32 v255, v255, v253
	v_fma_f32 v19, v249, v15, v19
	v_fma_f32 v19, v255, v16, v19
	v_mul_f32_e32 v244, v86, v90
	v_mul_f32_e32 v250, v87, v91
	v_mul_f32_e64 v245, -v90, v90
	v_mul_f32_e64 v251, -v91, v91
	v_add_f32_e32 v246, v86, v90
	v_add_f32_e32 v252, v87, v91
	v_fma_f32 v245, -v86, v86, v245
	v_fma_f32 v251, -v87, v87, v251
	v_fma_f32 v247, v10, v246, v11
	v_fma_f32 v253, v10, v252, v11
	v_fma_f32 v246, v13, v98, v14
	v_fma_f32 v252, v13, v99, v14
	v_fma_f32 v248, v12, v94, v245
	v_fma_f32 v254, v12, v95, v251
	v_fma_f32 v249, 2.0, v244, v247
	v_fma_f32 v255, 2.0, v250, v253
	v_sub_f32_e32 v247, v247, v245
	v_sub_f32_e32 v253, v253, v251
	v_fma_f32 v246, -2.0, v244, v246
	v_fma_f32 v252, -2.0, v250, v252
	v_mul_f32_e32 v247, v247, v248
	v_mul_f32_e32 v253, v253, v254
	v_rcp_f32_e32 v247, v247
	v_rcp_f32_e32 v253, v253
	v_mul_f32_e32 v249, v249, v246
	v_mul_f32_e32 v255, v255, v252
	v_mul_f32_e32 v249, v249, v247
	v_mul_f32_e32 v255, v255, v253
	v_fma_f32 v20, v249, v17, v20
	v_fma_f32 v20, v255, v18, v20
	s_waitcnt vmcnt(12)
	v_cvt_pk_f16_f32 v36, v100, v104
	v_cvt_pk_f16_f32 v52, v132, v136
	v_pk_add_f16 v36, v36, -0.5 op_sel_hi:[1,0]
	v_pk_add_f16 v52, v52, -0.5 op_sel_hi:[1,0]
	v_pk_mul_f16 v68, v52, v52
	v_pk_mul_f16 v84, v36, v52
	v_pk_fma_f16 v68, v36, v36, v68
	v_cvt_pk_f16_f32 v40, v101, v105
	v_cvt_pk_f16_f32 v56, v133, v137
	v_pk_add_f16 v40, v40, -0.5 op_sel_hi:[1,0]
	v_pk_add_f16 v56, v56, -0.5 op_sel_hi:[1,0]
	v_pk_mul_f16 v72, v56, v56
	v_pk_mul_f16 v88, v40, v56
	v_pk_fma_f16 v72, v40, v40, v72
	v_cvt_pk_f16_f32 v44, v102, v106
	v_cvt_pk_f16_f32 v60, v134, v138
	v_pk_add_f16 v44, v44, -0.5 op_sel_hi:[1,0]
	v_pk_add_f16 v60, v60, -0.5 op_sel_hi:[1,0]
	v_pk_mul_f16 v76, v60, v60
	v_pk_mul_f16 v92, v44, v60
	v_pk_fma_f16 v76, v44, v44, v76
	v_cvt_pk_f16_f32 v48, v103, v107
	v_cvt_pk_f16_f32 v64, v135, v139
	v_pk_add_f16 v48, v48, -0.5 op_sel_hi:[1,0]
	v_pk_add_f16 v64, v64, -0.5 op_sel_hi:[1,0]
	v_pk_mul_f16 v80, v64, v64
	v_pk_mul_f16 v96, v48, v64
	v_pk_fma_f16 v80, v48, v48, v80
	s_waitcnt vmcnt(8)
	v_cvt_pk_f16_f32 v37, v108, v112
	v_cvt_pk_f16_f32 v53, v140, v144
	v_pk_add_f16 v37, v37, -0.5 op_sel_hi:[1,0]
	v_pk_add_f16 v53, v53, -0.5 op_sel_hi:[1,0]
	v_pk_mul_f16 v69, v53, v53
	v_pk_mul_f16 v85, v37, v53
	v_pk_fma_f16 v69, v37, v37, v69
	v_cvt_pk_f16_f32 v41, v109, v113
	v_cvt_pk_f16_f32 v57, v141, v145
	v_pk_add_f16 v41, v41, -0.5 op_sel_hi:[1,0]
	v_pk_add_f16 v57, v57, -0.5 op_sel_hi:[1,0]
	v_pk_mul_f16 v73, v57, v57
	v_pk_mul_f16 v89, v41, v57
	v_pk_fma_f16 v73, v41, v41, v73
	v_cvt_pk_f16_f32 v45, v110, v114
	v_cvt_pk_f16_f32 v61, v142, v146
	v_pk_add_f16 v45, v45, -0.5 op_sel_hi:[1,0]
	v_pk_add_f16 v61, v61, -0.5 op_sel_hi:[1,0]
	v_pk_mul_f16 v77, v61, v61
	v_pk_mul_f16 v93, v45, v61
	v_pk_fma_f16 v77, v45, v45, v77
	v_cvt_pk_f16_f32 v49, v111, v115
	v_cvt_pk_f16_f32 v65, v143, v147
	v_pk_add_f16 v49, v49, -0.5 op_sel_hi:[1,0]
	v_pk_add_f16 v65, v65, -0.5 op_sel_hi:[1,0]
	v_pk_mul_f16 v81, v65, v65
	v_pk_mul_f16 v97, v49, v65
	v_pk_fma_f16 v81, v49, v49, v81
	s_waitcnt vmcnt(4)
	v_cvt_pk_f16_f32 v38, v116, v120
	v_cvt_pk_f16_f32 v54, v148, v152
	v_pk_add_f16 v38, v38, -0.5 op_sel_hi:[1,0]
	v_pk_add_f16 v54, v54, -0.5 op_sel_hi:[1,0]
	v_pk_mul_f16 v70, v54, v54
	v_pk_mul_f16 v86, v38, v54
	v_pk_fma_f16 v70, v38, v38, v70
	v_cvt_pk_f16_f32 v42, v117, v121
	v_cvt_pk_f16_f32 v58, v149, v153
	v_pk_add_f16 v42, v42, -0.5 op_sel_hi:[1,0]
	v_pk_add_f16 v58, v58, -0.5 op_sel_hi:[1,0]
	v_pk_mul_f16 v74, v58, v58
	v_pk_mul_f16 v90, v42, v58
	v_pk_fma_f16 v74, v42, v42, v74
	v_cvt_pk_f16_f32 v46, v118, v122
	v_cvt_pk_f16_f32 v62, v150, v154
	v_pk_add_f16 v46, v46, -0.5 op_sel_hi:[1,0]
	v_pk_add_f16 v62, v62, -0.5 op_sel_hi:[1,0]
	v_pk_mul_f16 v78, v62, v62
	v_pk_mul_f16 v94, v46, v62
	v_pk_fma_f16 v78, v46, v46, v78
	v_cvt_pk_f16_f32 v50, v119, v123
	v_cvt_pk_f16_f32 v66, v151, v155
	v_pk_add_f16 v50, v50, -0.5 op_sel_hi:[1,0]
	v_pk_add_f16 v66, v66, -0.5 op_sel_hi:[1,0]
	v_pk_mul_f16 v82, v66, v66
	v_pk_mul_f16 v98, v50, v66
	v_pk_fma_f16 v82, v50, v50, v82
	s_waitcnt vmcnt(0)
	v_cvt_pk_f16_f32 v39, v124, v128
	v_cvt_pk_f16_f32 v55, v156, v160
	v_pk_add_f16 v39, v39, -0.5 op_sel_hi:[1,0]
	v_pk_add_f16 v55, v55, -0.5 op_sel_hi:[1,0]
	v_pk_mul_f16 v71, v55, v55
	v_pk_mul_f16 v87, v39, v55
	v_pk_fma_f16 v71, v39, v39, v71
	v_cvt_pk_f16_f32 v43, v125, v129
	v_cvt_pk_f16_f32 v59, v157, v161
	v_pk_add_f16 v43, v43, -0.5 op_sel_hi:[1,0]
	v_pk_add_f16 v59, v59, -0.5 op_sel_hi:[1,0]
	v_pk_mul_f16 v75, v59, v59
	v_pk_mul_f16 v91, v43, v59
	v_pk_fma_f16 v75, v43, v43, v75
	v_cvt_pk_f16_f32 v47, v126, v130
	v_cvt_pk_f16_f32 v63, v158, v162
	v_pk_add_f16 v47, v47, -0.5 op_sel_hi:[1,0]
	v_pk_add_f16 v63, v63, -0.5 op_sel_hi:[1,0]
	v_pk_mul_f16 v79, v63, v63
	v_pk_mul_f16 v95, v47, v63
	v_pk_fma_f16 v79, v47, v47, v79
	v_cvt_pk_f16_f32 v51, v127, v131
	v_cvt_pk_f16_f32 v67, v159, v163
	v_pk_add_f16 v51, v51, -0.5 op_sel_hi:[1,0]
	v_pk_add_f16 v67, v67, -0.5 op_sel_hi:[1,0]
	v_pk_mul_f16 v83, v67, v67
	v_pk_mul_f16 v99, v51, v67
	v_pk_fma_f16 v83, v51, v51, v83
	v_mfma_f32_16x16x32_f16 v[132:135], v[164:167], v[28:31], 0
	v_mfma_f32_16x16x32_f16 v[136:139], v[168:171], v[28:31], 0
	v_mfma_f32_16x16x32_f16 v[140:143], v[172:175], v[28:31], 0
	v_mfma_f32_16x16x32_f16 v[144:147], v[176:179], v[28:31], 0
	v_mfma_f32_16x16x32_f16 v[132:135], v[36:39], v[32:35], v[132:135]
	v_mfma_f32_16x16x32_f16 v[136:139], v[40:43], v[32:35], v[136:139]
	v_mfma_f32_16x16x32_f16 v[140:143], v[44:47], v[32:35], v[140:143]
	v_mfma_f32_16x16x32_f16 v[144:147], v[48:51], v[32:35], v[144:147]
	v_mfma_f32_16x16x32_f16 v[148:151], v[180:183], v[28:31], 0
	v_mfma_f32_16x16x32_f16 v[152:155], v[184:187], v[28:31], 0
	v_mfma_f32_16x16x32_f16 v[156:159], v[188:191], v[28:31], 0
	v_mfma_f32_16x16x32_f16 v[160:163], v[192:195], v[28:31], 0
	v_mfma_f32_16x16x32_f16 v[148:151], v[52:55], v[32:35], v[148:151]
	v_mfma_f32_16x16x32_f16 v[152:155], v[56:59], v[32:35], v[152:155]
	v_mfma_f32_16x16x32_f16 v[156:159], v[60:63], v[32:35], v[156:159]
	v_mfma_f32_16x16x32_f16 v[160:163], v[64:67], v[32:35], v[160:163]
	v_cvt_pk_f16_f32 v100, v132, v136
	v_cvt_pk_f16_f32 v101, v140, v144
	v_cvt_pk_f16_f32 v102, v133, v137
	v_cvt_pk_f16_f32 v103, v141, v145
	v_cvt_pk_f16_f32 v104, v134, v138
	v_cvt_pk_f16_f32 v105, v142, v146
	v_cvt_pk_f16_f32 v106, v135, v139
	v_cvt_pk_f16_f32 v107, v143, v147
	v_mfma_f32_16x16x32_f16 v[132:135], v[196:199], v[28:31], 0
	v_mfma_f32_16x16x32_f16 v[136:139], v[200:203], v[28:31], 0
	v_mfma_f32_16x16x32_f16 v[140:143], v[204:207], v[28:31], 0
	v_mfma_f32_16x16x32_f16 v[144:147], v[208:211], v[28:31], 0
	v_mfma_f32_16x16x32_f16 v[132:135], v[68:71], v[32:35], v[132:135]
	v_mfma_f32_16x16x32_f16 v[136:139], v[72:75], v[32:35], v[136:139]
	v_mfma_f32_16x16x32_f16 v[140:143], v[76:79], v[32:35], v[140:143]
	v_mfma_f32_16x16x32_f16 v[144:147], v[80:83], v[32:35], v[144:147]
	v_cvt_pk_f16_f32 v108, v148, v152
	v_cvt_pk_f16_f32 v109, v156, v160
	v_cvt_pk_f16_f32 v110, v149, v153
	v_cvt_pk_f16_f32 v111, v157, v161
	v_cvt_pk_f16_f32 v112, v150, v154
	v_cvt_pk_f16_f32 v113, v158, v162
	v_cvt_pk_f16_f32 v114, v151, v155
	v_cvt_pk_f16_f32 v115, v159, v163
	v_mfma_f32_16x16x32_f16 v[148:151], v[212:215], v[28:31], 0
	v_mfma_f32_16x16x32_f16 v[152:155], v[216:219], v[28:31], 0
	v_mfma_f32_16x16x32_f16 v[156:159], v[220:223], v[28:31], 0
	v_mfma_f32_16x16x32_f16 v[160:163], v[224:227], v[28:31], 0
	v_mfma_f32_16x16x32_f16 v[148:151], v[84:87], v[32:35], v[148:151]
	v_mfma_f32_16x16x32_f16 v[152:155], v[88:91], v[32:35], v[152:155]
	v_mfma_f32_16x16x32_f16 v[156:159], v[92:95], v[32:35], v[156:159]
	v_mfma_f32_16x16x32_f16 v[160:163], v[96:99], v[32:35], v[160:163]
	v_cvt_pk_f16_f32 v116, v132, v136
	v_cvt_pk_f16_f32 v117, v140, v144
	v_cvt_pk_f16_f32 v118, v133, v137
	v_cvt_pk_f16_f32 v119, v141, v145
	v_cvt_pk_f16_f32 v120, v134, v138
	v_cvt_pk_f16_f32 v121, v142, v146
	v_cvt_pk_f16_f32 v122, v135, v139
	v_cvt_pk_f16_f32 v123, v143, v147
	v_cvt_pk_f16_f32 v124, v148, v152
	v_cvt_pk_f16_f32 v125, v156, v160
	v_cvt_pk_f16_f32 v126, v149, v153
	v_cvt_pk_f16_f32 v127, v157, v161
	v_cvt_pk_f16_f32 v128, v150, v154
	v_cvt_pk_f16_f32 v129, v158, v162
	v_cvt_pk_f16_f32 v130, v151, v155
	v_cvt_pk_f16_f32 v131, v159, v163
	global_load_dwordx4 v[164:167], v23, s[84:85] offset:0 nt
	global_load_dwordx4 v[168:171], v23, s[84:85] offset:2048 nt
	global_load_dwordx4 v[180:183], v23, s[88:89] offset:0 nt
	global_load_dwordx4 v[184:187], v23, s[88:89] offset:2048 nt
	global_load_dwordx4 v[172:175], v23, s[86:87] offset:0 nt
	global_load_dwordx4 v[176:179], v23, s[86:87] offset:2048 nt
	global_load_dwordx4 v[188:191], v23, s[90:91] offset:0 nt
	global_load_dwordx4 v[192:195], v23, s[90:91] offset:2048 nt
	s_mov_b64 exec, s[38:39]
	ds_write_b128 v4, v[104:107] offset:16384
	ds_write_b128 v4, v[112:115] offset:16896
	ds_write_b128 v4, v[120:123] offset:17408
	ds_write_b128 v4, v[128:131] offset:17920
	s_mov_b64 exec, -1
	v_mfma_f32_16x16x32_f16 v[132:135], v[24:27], v[100:103], 0
	v_mfma_f32_16x16x32_f16 v[136:139], v[24:27], v[108:111], 0
	v_mfma_f32_16x16x32_f16 v[140:143], v[24:27], v[116:119], v[0:3]
	v_mfma_f32_16x16x32_f16 v[144:147], v[24:27], v[124:127], 0
	v_mfma_f32_16x16x32_f16 v[148:151], v[28:31], v[100:103], 0
	v_mfma_f32_16x16x32_f16 v[152:155], v[28:31], v[108:111], 0
	v_mfma_f32_16x16x32_f16 v[156:159], v[28:31], v[116:119], v[0:3]
	v_mfma_f32_16x16x32_f16 v[160:163], v[28:31], v[124:127], 0
	v_mfma_f32_16x16x32_f16 v[148:151], v[32:35], v[104:107], v[148:151]
	v_mfma_f32_16x16x32_f16 v[152:155], v[32:35], v[112:115], v[152:155]
	v_mfma_f32_16x16x32_f16 v[156:159], v[32:35], v[120:123], v[156:159]
	v_mfma_f32_16x16x32_f16 v[160:163], v[32:35], v[128:131], v[160:163]
	s_waitcnt lgkmcnt(0)
	ds_write_b32 v6, v6 offset:32
	ds_read_b32 v9, v7 offset:32
	v_mul_f32_e32 v244, v132, v136
	v_mul_f32_e32 v250, v133, v137
	v_mul_f32_e64 v245, -v136, v136
	v_mul_f32_e64 v251, -v137, v137
	v_add_f32_e32 v246, v132, v136
	v_add_f32_e32 v252, v133, v137
	v_fma_f32 v245, -v132, v132, v245
	v_fma_f32 v251, -v133, v133, v251
	v_fma_f32 v247, v10, v246, v11
	v_fma_f32 v253, v10, v252, v11
	v_fma_f32 v246, v13, v144, v14
	v_fma_f32 v252, v13, v145, v14
	v_fma_f32 v248, v12, v140, v245
	v_fma_f32 v254, v12, v141, v251
	v_fma_f32 v249, 2.0, v244, v247
	v_fma_f32 v255, 2.0, v250, v253
	v_sub_f32_e32 v247, v247, v245
	v_sub_f32_e32 v253, v253, v251
	v_fma_f32 v246, -2.0, v244, v246
	v_fma_f32 v252, -2.0, v250, v252
	v_mul_f32_e32 v247, v247, v248
	v_mul_f32_e32 v253, v253, v254
	v_rcp_f32_e32 v247, v247
	v_rcp_f32_e32 v253, v253
	v_mul_f32_e32 v249, v249, v246
	v_mul_f32_e32 v255, v255, v252
	v_fma_f32 v19, v249, v247, v19
	v_fma_f32 v19, v255, v253, v19
	v_mul_f32_e32 v244, v134, v138
	v_mul_f32_e32 v250, v135, v139
	v_mul_f32_e64 v245, -v138, v138
	v_mul_f32_e64 v251, -v139, v139
	v_add_f32_e32 v246, v134, v138
	v_add_f32_e32 v252, v135, v139
	v_fma_f32 v245, -v134, v134, v245
	v_fma_f32 v251, -v135, v135, v251
	v_fma_f32 v247, v10, v246, v11
	v_fma_f32 v253, v10, v252, v11
	v_fma_f32 v246, v13, v146, v14
	v_fma_f32 v252, v13, v147, v14
	v_fma_f32 v248, v12, v142, v245
	v_fma_f32 v254, v12, v143, v251
	v_fma_f32 v249, 2.0, v244, v247
	v_fma_f32 v255, 2.0, v250, v253
	v_sub_f32_e32 v247, v247, v245
	v_sub_f32_e32 v253, v253, v251
	v_fma_f32 v246, -2.0, v244, v246
	v_fma_f32 v252, -2.0, v250, v252
	v_mul_f32_e32 v247, v247, v248
	v_mul_f32_e32 v253, v253, v254
	v_rcp_f32_e32 v247, v247
	v_rcp_f32_e32 v253, v253
	v_mul_f32_e32 v249, v249, v246
	v_mul_f32_e32 v255, v255, v252
	v_fma_f32 v20, v249, v247, v20
	v_fma_f32 v20, v255, v253, v20
	v_mfma_f32_16x16x32_f16 v[132:135], v[24:27], v[104:107], 0
	v_mfma_f32_16x16x32_f16 v[136:139], v[24:27], v[112:115], 0
	v_mfma_f32_16x16x32_f16 v[140:143], v[24:27], v[120:123], v[0:3]
	v_mfma_f32_16x16x32_f16 v[144:147], v[24:27], v[128:131], 0
	s_waitcnt lgkmcnt(0)
	v_cmp_ne_u32_e32 vcc, 0, v9
	s_cbranch_vccnz .Lq_go_1

.Lq_go_2:
	ds_read_b128 v[228:231], v5 offset:32768
	ds_read_b128 v[232:235], v5 offset:33280
	ds_read_b128 v[236:239], v5 offset:33792
	ds_read_b128 v[240:243], v5 offset:34304
	v_mul_f32_e32 v244, v148, v152
	v_mul_f32_e32 v250, v149, v153
	v_mul_f32_e64 v245, -v152, v152
	v_mul_f32_e64 v251, -v153, v153
	v_add_f32_e32 v246, v148, v152
	v_add_f32_e32 v252, v149, v153
	v_fma_f32 v245, -v148, v148, v245
	v_fma_f32 v251, -v149, v149, v251
	v_fma_f32 v247, v10, v246, v11
	v_fma_f32 v253, v10, v252, v11
	v_fma_f32 v246, v13, v160, v14
	v_fma_f32 v252, v13, v161, v14
	v_fma_f32 v248, v12, v156, v245
	v_fma_f32 v254, v12, v157, v251
	v_fma_f32 v249, 2.0, v244, v247
	v_fma_f32 v255, 2.0, v250, v253
	v_sub_f32_e32 v247, v247, v245
	v_sub_f32_e32 v253, v253, v251
	v_fma_f32 v246, -2.0, v244, v246
	v_fma_f32 v252, -2.0, v250, v252
	v_mul_f32_e32 v247, v247, v248
	v_mul_f32_e32 v253, v253, v254
	v_rcp_f32_e32 v247, v247
	v_rcp_f32_e32 v253, v253
	v_mul_f32_e32 v249, v249, v246
	v_mul_f32_e32 v255, v255, v252
	v_fma_f32 v19, v249, v247, v19
	v_fma_f32 v19, v255, v253, v19
	v_mul_f32_e32 v244, v150, v154
	v_mul_f32_e32 v250, v151, v155
	v_mul_f32_e64 v245, -v154, v154
	v_mul_f32_e64 v251, -v155, v155
	v_add_f32_e32 v246, v150, v154
	v_add_f32_e32 v252, v151, v155
	v_fma_f32 v245, -v150, v150, v245
	v_fma_f32 v251, -v151, v151, v251
	v_fma_f32 v247, v10, v246, v11
	v_fma_f32 v253, v10, v252, v11
	v_fma_f32 v246, v13, v162, v14
	v_fma_f32 v252, v13, v163, v14
	v_fma_f32 v248, v12, v158, v245
	v_fma_f32 v254, v12, v159, v251
	v_fma_f32 v249, 2.0, v244, v247
	v_fma_f32 v255, 2.0, v250, v253
	v_sub_f32_e32 v247, v247, v245
	v_sub_f32_e32 v253, v253, v251
	v_fma_f32 v246, -2.0, v244, v246
	v_fma_f32 v252, -2.0, v250, v252
	v_mul_f32_e32 v247, v247, v248
	v_mul_f32_e32 v253, v253, v254
	v_rcp_f32_e32 v247, v247
	v_rcp_f32_e32 v253, v253
	v_mul_f32_e32 v249, v249, v246
	v_mul_f32_e32 v255, v255, v252
	v_fma_f32 v20, v249, v247, v20
	v_fma_f32 v20, v255, v253, v20
	s_waitcnt lgkmcnt(0)
	v_mfma_f32_16x16x32_f16 v[148:151], v[28:31], v[228:231], 0
	v_mfma_f32_16x16x32_f16 v[152:155], v[28:31], v[232:235], 0
	v_mfma_f32_16x16x32_f16 v[156:159], v[28:31], v[236:239], v[0:3]
	v_mfma_f32_16x16x32_f16 v[160:163], v[28:31], v[240:243], 0
	v_mfma_f32_16x16x32_f16 v[148:151], v[32:35], v[100:103], v[148:151]
	v_mfma_f32_16x16x32_f16 v[152:155], v[32:35], v[108:111], v[152:155]
	v_mfma_f32_16x16x32_f16 v[156:159], v[32:35], v[116:119], v[156:159]
	v_mfma_f32_16x16x32_f16 v[160:163], v[32:35], v[124:127], v[160:163]
	v_mul_f32_e32 v244, v132, v136
	v_mul_f32_e32 v250, v133, v137
	v_mul_f32_e64 v245, -v136, v136
	v_mul_f32_e64 v251, -v137, v137
	v_add_f32_e32 v246, v132, v136
	v_add_f32_e32 v252, v133, v137
	v_fma_f32 v245, -v132, v132, v245
	v_fma_f32 v251, -v133, v133, v251
	v_fma_f32 v247, v10, v246, v11
	v_fma_f32 v253, v10, v252, v11
	v_fma_f32 v246, v13, v144, v14
	v_fma_f32 v252, v13, v145, v14
	v_fma_f32 v248, v12, v140, v245
	v_fma_f32 v254, v12, v141, v251
	v_fma_f32 v249, 2.0, v244, v247
	v_fma_f32 v255, 2.0, v250, v253
	v_sub_f32_e32 v247, v247, v245
	v_sub_f32_e32 v253, v253, v251
	v_fma_f32 v246, -2.0, v244, v246
	v_fma_f32 v252, -2.0, v250, v252
	v_mul_f32_e32 v247, v247, v248
	v_mul_f32_e32 v253, v253, v254
	v_rcp_f32_e32 v247, v247
	v_rcp_f32_e32 v253, v253
	v_mul_f32_e32 v249, v249, v246
	v_mul_f32_e32 v255, v255, v252
	v_fma_f32 v19, v249, v247, v19
	v_fma_f32 v19, v255, v253, v19
	v_mul_f32_e32 v244, v134, v138
	v_mul_f32_e32 v250, v135, v139
	v_mul_f32_e64 v245, -v138, v138
	v_mul_f32_e64 v251, -v139, v139
	v_add_f32_e32 v246, v134, v138
	v_add_f32_e32 v252, v135, v139
	v_fma_f32 v245, -v134, v134, v245
	v_fma_f32 v251, -v135, v135, v251
	v_fma_f32 v247, v10, v246, v11
	v_fma_f32 v253, v10, v252, v11
	v_fma_f32 v246, v13, v146, v14
	v_fma_f32 v252, v13, v147, v14
	v_fma_f32 v248, v12, v142, v245
	v_fma_f32 v254, v12, v143, v251
	v_fma_f32 v249, 2.0, v244, v247
	v_fma_f32 v255, 2.0, v250, v253
	v_sub_f32_e32 v247, v247, v245
	v_sub_f32_e32 v253, v253, v251
	v_fma_f32 v246, -2.0, v244, v246
	v_fma_f32 v252, -2.0, v250, v252
	v_mul_f32_e32 v247, v247, v248
	v_mul_f32_e32 v253, v253, v254
	v_rcp_f32_e32 v247, v247
	v_rcp_f32_e32 v253, v253
	v_mul_f32_e32 v249, v249, v246
	v_mul_f32_e32 v255, v255, v252
	v_fma_f32 v20, v249, v247, v20
	v_fma_f32 v20, v255, v253, v20
	v_mul_f32_e32 v244, v148, v152
	v_mul_f32_e32 v250, v149, v153
	v_mul_f32_e64 v245, -v152, v152
	v_mul_f32_e64 v251, -v153, v153
	v_add_f32_e32 v246, v148, v152
	v_add_f32_e32 v252, v149, v153
	v_fma_f32 v245, -v148, v148, v245
	v_fma_f32 v251, -v149, v149, v251
	v_fma_f32 v247, v10, v246, v11
	v_fma_f32 v253, v10, v252, v11
	v_fma_f32 v246, v13, v160, v14
	v_fma_f32 v252, v13, v161, v14
	v_fma_f32 v248, v12, v156, v245
	v_fma_f32 v254, v12, v157, v251
	v_fma_f32 v249, 2.0, v244, v247
	v_fma_f32 v255, 2.0, v250, v253
	v_sub_f32_e32 v247, v247, v245
	v_sub_f32_e32 v253, v253, v251
	v_fma_f32 v246, -2.0, v244, v246
	v_fma_f32 v252, -2.0, v250, v252
	v_mul_f32_e32 v247, v247, v248
	v_mul_f32_e32 v253, v253, v254
	v_rcp_f32_e32 v247, v247
	v_rcp_f32_e32 v253, v253
	v_mul_f32_e32 v249, v249, v246
	v_mul_f32_e32 v255, v255, v252
	v_mul_f32_e32 v249, v249, v247
	v_mul_f32_e32 v255, v255, v253
	v_fma_f32 v19, v249, v15, v19
	v_fma_f32 v19, v255, v16, v19
	v_mul_f32_e32 v244, v150, v154
	v_mul_f32_e32 v250, v151, v155
	v_mul_f32_e64 v245, -v154, v154
	v_mul_f32_e64 v251, -v155, v155
	v_add_f32_e32 v246, v150, v154
	v_add_f32_e32 v252, v151, v155
	v_fma_f32 v245, -v150, v150, v245
	v_fma_f32 v251, -v151, v151, v251
	v_fma_f32 v247, v10, v246, v11
	v_fma_f32 v253, v10, v252, v11
	v_fma_f32 v246, v13, v162, v14
	v_fma_f32 v252, v13, v163, v14
	v_fma_f32 v248, v12, v158, v245
	v_fma_f32 v254, v12, v159, v251
	v_fma_f32 v249, 2.0, v244, v247
	v_fma_f32 v255, 2.0, v250, v253
	v_sub_f32_e32 v247, v247, v245
	v_sub_f32_e32 v253, v253, v251
	v_fma_f32 v246, -2.0, v244, v246
	v_fma_f32 v252, -2.0, v250, v252
	v_mul_f32_e32 v247, v247, v248
	v_mul_f32_e32 v253, v253, v254
	v_rcp_f32_e32 v247, v247
	v_rcp_f32_e32 v253, v253
	v_mul_f32_e32 v249, v249, v246
	v_mul_f32_e32 v255, v255, v252
	v_mul_f32_e32 v249, v249, v247
	v_mul_f32_e32 v255, v255, v253
	v_fma_f32 v20, v249, v17, v20
	v_fma_f32 v20, v255, v18, v20
	s_waitcnt vmcnt(4)
	v_cvt_pk_f16_f32 v100, v164, v168
	v_cvt_pk_f16_f32 v116, v180, v184
	v_pk_add_f16 v100, v100, -0.5 op_sel_hi:[1,0]
	v_pk_add_f16 v116, v116, -0.5 op_sel_hi:[1,0]
	v_pk_mul_f16 v132, v116, v116
	v_pk_mul_f16 v148, v100, v116
	v_pk_fma_f16 v132, v100, v100, v132
	v_cvt_pk_f16_f32 v104, v165, v169
	v_cvt_pk_f16_f32 v120, v181, v185
	v_pk_add_f16 v104, v104, -0.5 op_sel_hi:[1,0]
	v_pk_add_f16 v120, v120, -0.5 op_sel_hi:[1,0]
	v_pk_mul_f16 v136, v120, v120
	v_pk_mul_f16 v152, v104, v120
	v_pk_fma_f16 v136, v104, v104, v136
	v_cvt_pk_f16_f32 v108, v166, v170
	v_cvt_pk_f16_f32 v124, v182, v186
	v_pk_add_f16 v108, v108, -0.5 op_sel_hi:[1,0]
	v_pk_add_f16 v124, v124, -0.5 op_sel_hi:[1,0]
	v_pk_mul_f16 v140, v124, v124
	v_pk_mul_f16 v156, v108, v124
	v_pk_fma_f16 v140, v108, v108, v140
	v_cvt_pk_f16_f32 v112, v167, v171
	v_cvt_pk_f16_f32 v128, v183, v187
	v_pk_add_f16 v112, v112, -0.5 op_sel_hi:[1,0]
	v_pk_add_f16 v128, v128, -0.5 op_sel_hi:[1,0]
	v_pk_mul_f16 v144, v128, v128
	v_pk_mul_f16 v160, v112, v128
	v_pk_fma_f16 v144, v112, v112, v144
	s_waitcnt vmcnt(0)
	v_cvt_pk_f16_f32 v101, v172, v176
	v_cvt_pk_f16_f32 v117, v188, v192
	v_pk_add_f16 v101, v101, -0.5 op_sel_hi:[1,0]
	v_pk_add_f16 v117, v117, -0.5 op_sel_hi:[1,0]
	v_pk_mul_f16 v133, v117, v117
	v_pk_mul_f16 v149, v101, v117
	v_pk_fma_f16 v133, v101, v101, v133
	v_cvt_pk_f16_f32 v105, v173, v177
	v_cvt_pk_f16_f32 v121, v189, v193
	v_pk_add_f16 v105, v105, -0.5 op_sel_hi:[1,0]
	v_pk_add_f16 v121, v121, -0.5 op_sel_hi:[1,0]
	v_pk_mul_f16 v137, v121, v121
	v_pk_mul_f16 v153, v105, v121
	v_pk_fma_f16 v137, v105, v105, v137
	v_cvt_pk_f16_f32 v109, v174, v178
	v_cvt_pk_f16_f32 v125, v190, v194
	v_pk_add_f16 v109, v109, -0.5 op_sel_hi:[1,0]
	v_pk_add_f16 v125, v125, -0.5 op_sel_hi:[1,0]
	v_pk_mul_f16 v141, v125, v125
	v_pk_mul_f16 v157, v109, v125
	v_pk_fma_f16 v141, v109, v109, v141
	v_cvt_pk_f16_f32 v113, v175, v179
	v_cvt_pk_f16_f32 v129, v191, v195
	v_pk_add_f16 v113, v113, -0.5 op_sel_hi:[1,0]
	v_pk_add_f16 v129, v129, -0.5 op_sel_hi:[1,0]
	v_pk_mul_f16 v145, v129, v129
	v_pk_mul_f16 v161, v113, v129
	v_pk_fma_f16 v145, v113, v113, v145
	v_xor_b32_e32 v23, 32, v8
	v_lshlrev_b32_e32 v23, 2, v23
	ds_bpermute_b32 v102, v23, v100
	ds_bpermute_b32 v103, v23, v101
	ds_bpermute_b32 v106, v23, v104
	ds_bpermute_b32 v107, v23, v105
	ds_bpermute_b32 v110, v23, v108
	ds_bpermute_b32 v111, v23, v109
	ds_bpermute_b32 v114, v23, v112
	ds_bpermute_b32 v115, v23, v113
	s_waitcnt lgkmcnt(0)
	ds_bpermute_b32 v118, v23, v116
	ds_bpermute_b32 v119, v23, v117
	ds_bpermute_b32 v122, v23, v120
	ds_bpermute_b32 v123, v23, v121
	ds_bpermute_b32 v126, v23, v124
	ds_bpermute_b32 v127, v23, v125
	ds_bpermute_b32 v130, v23, v128
	ds_bpermute_b32 v131, v23, v129
	s_waitcnt lgkmcnt(0)
	ds_bpermute_b32 v134, v23, v132
	ds_bpermute_b32 v135, v23, v133
	ds_bpermute_b32 v138, v23, v136
	ds_bpermute_b32 v139, v23, v137
	ds_bpermute_b32 v142, v23, v140
	ds_bpermute_b32 v143, v23, v141
	ds_bpermute_b32 v146, v23, v144
	ds_bpermute_b32 v147, v23, v145
	s_waitcnt lgkmcnt(0)
	ds_bpermute_b32 v150, v23, v148
	ds_bpermute_b32 v151, v23, v149
	ds_bpermute_b32 v154, v23, v152
	ds_bpermute_b32 v155, v23, v153
	ds_bpermute_b32 v158, v23, v156
	ds_bpermute_b32 v159, v23, v157
	ds_bpermute_b32 v162, v23, v160
	ds_bpermute_b32 v163, v23, v161
	s_waitcnt lgkmcnt(0)
	v_mfma_f32_16x16x32_f16 v[196:199], v[36:39], v[28:31], 0
	v_mfma_f32_16x16x32_f16 v[200:203], v[40:43], v[28:31], 0
	v_mfma_f32_16x16x32_f16 v[204:207], v[44:47], v[28:31], 0
	v_mfma_f32_16x16x32_f16 v[208:211], v[48:51], v[28:31], 0
	v_mfma_f32_16x16x32_f16 v[196:199], v[100:103], v[32:35], v[196:199]
	v_mfma_f32_16x16x32_f16 v[200:203], v[104:107], v[32:35], v[200:203]
	v_mfma_f32_16x16x32_f16 v[204:207], v[108:111], v[32:35], v[204:207]
	v_mfma_f32_16x16x32_f16 v[208:211], v[112:115], v[32:35], v[208:211]
	v_mfma_f32_16x16x32_f16 v[212:215], v[52:55], v[28:31], 0
	v_mfma_f32_16x16x32_f16 v[216:219], v[56:59], v[28:31], 0
	v_mfma_f32_16x16x32_f16 v[220:223], v[60:63], v[28:31], 0
	v_mfma_f32_16x16x32_f16 v[224:227], v[64:67], v[28:31], 0
	v_mfma_f32_16x16x32_f16 v[212:215], v[116:119], v[32:35], v[212:215]
	v_mfma_f32_16x16x32_f16 v[216:219], v[120:123], v[32:35], v[216:219]
	v_mfma_f32_16x16x32_f16 v[220:223], v[124:127], v[32:35], v[220:223]
	v_mfma_f32_16x16x32_f16 v[224:227], v[128:131], v[32:35], v[224:227]
	v_cvt_pk_f16_f32 v164, v196, v200
	v_cvt_pk_f16_f32 v165, v204, v208
	v_cvt_pk_f16_f32 v166, v197, v201
	v_cvt_pk_f16_f32 v167, v205, v209
	v_cvt_pk_f16_f32 v168, v198, v202
	v_cvt_pk_f16_f32 v169, v206, v210
	v_cvt_pk_f16_f32 v170, v199, v203
	v_cvt_pk_f16_f32 v171, v207, v211
	v_mfma_f32_16x16x32_f16 v[196:199], v[68:71], v[28:31], 0
	v_mfma_f32_16x16x32_f16 v[200:203], v[72:75], v[28:31], 0
	v_mfma_f32_16x16x32_f16 v[204:207], v[76:79], v[28:31], 0
	v_mfma_f32_16x16x32_f16 v[208:211], v[80:83], v[28:31], 0
	v_mfma_f32_16x16x32_f16 v[196:199], v[132:135], v[32:35], v[196:199]
	v_mfma_f32_16x16x32_f16 v[200:203], v[136:139], v[32:35], v[200:203]
	v_mfma_f32_16x16x32_f16 v[204:207], v[140:143], v[32:35], v[204:207]
	v_mfma_f32_16x16x32_f16 v[208:211], v[144:147], v[32:35], v[208:211]
	v_cvt_pk_f16_f32 v172, v212, v216
	v_cvt_pk_f16_f32 v173, v220, v224
	v_cvt_pk_f16_f32 v174, v213, v217
	v_cvt_pk_f16_f32 v175, v221, v225
	v_cvt_pk_f16_f32 v176, v214, v218
	v_cvt_pk_f16_f32 v177, v222, v226
	v_cvt_pk_f16_f32 v178, v215, v219
	v_cvt_pk_f16_f32 v179, v223, v227
	v_mfma_f32_16x16x32_f16 v[212:215], v[84:87], v[28:31], 0
	v_mfma_f32_16x16x32_f16 v[216:219], v[88:91], v[28:31], 0
	v_mfma_f32_16x16x32_f16 v[220:223], v[92:95], v[28:31], 0
	v_mfma_f32_16x16x32_f16 v[224:227], v[96:99], v[28:31], 0
	v_mfma_f32_16x16x32_f16 v[212:215], v[148:151], v[32:35], v[212:215]
	v_mfma_f32_16x16x32_f16 v[216:219], v[152:155], v[32:35], v[216:219]
	v_mfma_f32_16x16x32_f16 v[220:223], v[156:159], v[32:35], v[220:223]
	v_mfma_f32_16x16x32_f16 v[224:227], v[160:163], v[32:35], v[224:227]
	v_cvt_pk_f16_f32 v180, v196, v200
	v_cvt_pk_f16_f32 v181, v204, v208
	v_cvt_pk_f16_f32 v182, v197, v201
	v_cvt_pk_f16_f32 v183, v205, v209
	v_cvt_pk_f16_f32 v184, v198, v202
	v_cvt_pk_f16_f32 v185, v206, v210
	v_cvt_pk_f16_f32 v186, v199, v203
	v_cvt_pk_f16_f32 v187, v207, v211
	v_cvt_pk_f16_f32 v188, v212, v216
	v_cvt_pk_f16_f32 v189, v220, v224
	v_cvt_pk_f16_f32 v190, v213, v217
	v_cvt_pk_f16_f32 v191, v221, v225
	v_cvt_pk_f16_f32 v192, v214, v218
	v_cvt_pk_f16_f32 v193, v222, v226
	v_cvt_pk_f16_f32 v194, v215, v219
	v_cvt_pk_f16_f32 v195, v223, v227
	s_mov_b64 exec, s[38:39]
	ds_write_b128 v4, v[168:171] offset:49152
	ds_write_b128 v4, v[176:179] offset:49664
	ds_write_b128 v4, v[184:187] offset:50176
	ds_write_b128 v4, v[192:195] offset:50688
	s_mov_b64 exec, -1
	v_mfma_f32_16x16x32_f16 v[196:199], v[24:27], v[164:167], 0
	v_mfma_f32_16x16x32_f16 v[200:203], v[24:27], v[172:175], 0
	v_mfma_f32_16x16x32_f16 v[204:207], v[24:27], v[180:183], v[0:3]
	v_mfma_f32_16x16x32_f16 v[208:211], v[24:27], v[188:191], 0
	v_mfma_f32_16x16x32_f16 v[212:215], v[28:31], v[164:167], 0
	v_mfma_f32_16x16x32_f16 v[216:219], v[28:31], v[172:175], 0
	v_mfma_f32_16x16x32_f16 v[220:223], v[28:31], v[180:183], v[0:3]
	v_mfma_f32_16x16x32_f16 v[224:227], v[28:31], v[188:191], 0
	v_mfma_f32_16x16x32_f16 v[212:215], v[32:35], v[168:171], v[212:215]
	v_mfma_f32_16x16x32_f16 v[216:219], v[32:35], v[176:179], v[216:219]
	v_mfma_f32_16x16x32_f16 v[220:223], v[32:35], v[184:187], v[220:223]
	v_mfma_f32_16x16x32_f16 v[224:227], v[32:35], v[192:195], v[224:227]
	s_waitcnt lgkmcnt(0)
	ds_write_b32 v6, v6 offset:96
	ds_read_b32 v9, v7 offset:96
	v_mul_f32_e32 v244, v196, v200
	v_mul_f32_e32 v250, v197, v201
	v_mul_f32_e64 v245, -v200, v200
	v_mul_f32_e64 v251, -v201, v201
	v_add_f32_e32 v246, v196, v200
	v_add_f32_e32 v252, v197, v201
	v_fma_f32 v245, -v196, v196, v245
	v_fma_f32 v251, -v197, v197, v251
	v_fma_f32 v247, v10, v246, v11
	v_fma_f32 v253, v10, v252, v11
	v_fma_f32 v246, v13, v208, v14
	v_fma_f32 v252, v13, v209, v14
	v_fma_f32 v248, v12, v204, v245
	v_fma_f32 v254, v12, v205, v251
	v_fma_f32 v249, 2.0, v244, v247
	v_fma_f32 v255, 2.0, v250, v253
	v_sub_f32_e32 v247, v247, v245
	v_sub_f32_e32 v253, v253, v251
	v_fma_f32 v246, -2.0, v244, v246
	v_fma_f32 v252, -2.0, v250, v252
	v_mul_f32_e32 v247, v247, v248
	v_mul_f32_e32 v253, v253, v254
	v_rcp_f32_e32 v247, v247
	v_rcp_f32_e32 v253, v253
	v_mul_f32_e32 v249, v249, v246
	v_mul_f32_e32 v255, v255, v252
	v_fma_f32 v21, v249, v247, v21
	v_fma_f32 v21, v255, v253, v21
	v_mul_f32_e32 v244, v198, v202
	v_mul_f32_e32 v250, v199, v203
	v_mul_f32_e64 v245, -v202, v202
	v_mul_f32_e64 v251, -v203, v203
	v_add_f32_e32 v246, v198, v202
	v_add_f32_e32 v252, v199, v203
	v_fma_f32 v245, -v198, v198, v245
	v_fma_f32 v251, -v199, v199, v251
	v_fma_f32 v247, v10, v246, v11
	v_fma_f32 v253, v10, v252, v11
	v_fma_f32 v246, v13, v210, v14
	v_fma_f32 v252, v13, v211, v14
	v_fma_f32 v248, v12, v206, v245
	v_fma_f32 v254, v12, v207, v251
	v_fma_f32 v249, 2.0, v244, v247
	v_fma_f32 v255, 2.0, v250, v253
	v_sub_f32_e32 v247, v247, v245
	v_sub_f32_e32 v253, v253, v251
	v_fma_f32 v246, -2.0, v244, v246
	v_fma_f32 v252, -2.0, v250, v252
	v_mul_f32_e32 v247, v247, v248
	v_mul_f32_e32 v253, v253, v254
	v_rcp_f32_e32 v247, v247
	v_rcp_f32_e32 v253, v253
	v_mul_f32_e32 v249, v249, v246
	v_mul_f32_e32 v255, v255, v252
	v_fma_f32 v22, v249, v247, v22
	v_fma_f32 v22, v255, v253, v22
	v_mfma_f32_16x16x32_f16 v[196:199], v[24:27], v[168:171], 0
	v_mfma_f32_16x16x32_f16 v[200:203], v[24:27], v[176:179], 0
	v_mfma_f32_16x16x32_f16 v[204:207], v[24:27], v[184:187], v[0:3]
	v_mfma_f32_16x16x32_f16 v[208:211], v[24:27], v[192:195], 0
	s_waitcnt lgkmcnt(0)
	v_cmp_ne_u32_e32 vcc, 0, v9
	s_cbranch_vccnz .Lq_go_3

_Z10ssim_finalPKfPf:
	s_load_dwordx4 s[4:7], s[0:1], 0x0
	v_lshlrev_b32_e32 v2, 4, v0
	v_mov_b32_e32 v3, 0
	s_waitcnt lgkmcnt(0)
	s_add_u32 s8, s4, 0x1000
	s_addc_u32 s9, s5, 0
	global_load_dwordx4 v[4:7], v2, s[4:5]
	global_load_dwordx4 v[8:11], v2, s[4:5] offset:1024
	global_load_dwordx4 v[12:15], v2, s[4:5] offset:2048
	global_load_dwordx4 v[16:19], v2, s[4:5] offset:3072
	global_load_dwordx4 v[20:23], v2, s[8:9]
	global_load_dwordx4 v[24:27], v2, s[8:9] offset:1024
	global_load_dwordx4 v[28:31], v2, s[8:9] offset:2048
	global_load_dwordx4 v[32:35], v2, s[8:9] offset:3072
	s_waitcnt vmcnt(7)
	v_cvt_f64_f32_e32 v[36:37], v4
	v_cvt_f64_f32_e32 v[38:39], v5
	v_cvt_f64_f32_e32 v[40:41], v6
	v_cvt_f64_f32_e32 v[42:43], v7
	v_add_f64 v[36:37], v[36:37], v[38:39]
	v_add_f64 v[40:41], v[40:41], v[42:43]
	v_add_f64 v[44:45], v[36:37], v[40:41]
	s_waitcnt vmcnt(6)
	v_cvt_f64_f32_e32 v[36:37], v8
	v_cvt_f64_f32_e32 v[38:39], v9
	v_cvt_f64_f32_e32 v[40:41], v10
	v_cvt_f64_f32_e32 v[42:43], v11
	v_add_f64 v[36:37], v[36:37], v[38:39]
	v_add_f64 v[40:41], v[40:41], v[42:43]
	v_add_f64 v[36:37], v[36:37], v[40:41]
	v_add_f64 v[44:45], v[44:45], v[36:37]
	s_waitcnt vmcnt(5)
	v_cvt_f64_f32_e32 v[36:37], v12
	v_cvt_f64_f32_e32 v[38:39], v13
	v_cvt_f64_f32_e32 v[40:41], v14
	v_cvt_f64_f32_e32 v[42:43], v15
	v_add_f64 v[36:37], v[36:37], v[38:39]
	v_add_f64 v[40:41], v[40:41], v[42:43]
	v_add_f64 v[36:37], v[36:37], v[40:41]
	v_add_f64 v[44:45], v[44:45], v[36:37]
	s_waitcnt vmcnt(4)
	v_cvt_f64_f32_e32 v[36:37], v16
	v_cvt_f64_f32_e32 v[38:39], v17
	v_cvt_f64_f32_e32 v[40:41], v18
	v_cvt_f64_f32_e32 v[42:43], v19
	v_add_f64 v[36:37], v[36:37], v[38:39]
	v_add_f64 v[40:41], v[40:41], v[42:43]
	v_add_f64 v[36:37], v[36:37], v[40:41]
	v_add_f64 v[44:45], v[44:45], v[36:37]
	s_waitcnt vmcnt(3)
	v_cvt_f64_f32_e32 v[36:37], v20
	v_cvt_f64_f32_e32 v[38:39], v21
	v_cvt_f64_f32_e32 v[40:41], v22
	v_cvt_f64_f32_e32 v[42:43], v23
	v_add_f64 v[36:37], v[36:37], v[38:39]
	v_add_f64 v[40:41], v[40:41], v[42:43]
	v_add_f64 v[36:37], v[36:37], v[40:41]
	v_add_f64 v[44:45], v[44:45], v[36:37]
	s_waitcnt vmcnt(2)
	v_cvt_f64_f32_e32 v[36:37], v24
	v_cvt_f64_f32_e32 v[38:39], v25
	v_cvt_f64_f32_e32 v[40:41], v26
	v_cvt_f64_f32_e32 v[42:43], v27
	v_add_f64 v[36:37], v[36:37], v[38:39]
	v_add_f64 v[40:41], v[40:41], v[42:43]
	v_add_f64 v[36:37], v[36:37], v[40:41]
	v_add_f64 v[44:45], v[44:45], v[36:37]
	s_waitcnt vmcnt(1)
	v_cvt_f64_f32_e32 v[36:37], v28
	v_cvt_f64_f32_e32 v[38:39], v29
	v_cvt_f64_f32_e32 v[40:41], v30
	v_cvt_f64_f32_e32 v[42:43], v31
	v_add_f64 v[36:37], v[36:37], v[38:39]
	v_add_f64 v[40:41], v[40:41], v[42:43]
	v_add_f64 v[36:37], v[36:37], v[40:41]
	v_add_f64 v[44:45], v[44:45], v[36:37]
	s_waitcnt vmcnt(0)
	v_cvt_f64_f32_e32 v[36:37], v32
	v_cvt_f64_f32_e32 v[38:39], v33
	v_cvt_f64_f32_e32 v[40:41], v34
	v_cvt_f64_f32_e32 v[42:43], v35
	v_add_f64 v[36:37], v[36:37], v[38:39]
	v_add_f64 v[40:41], v[40:41], v[42:43]
	v_add_f64 v[36:37], v[36:37], v[40:41]
	v_add_f64 v[44:45], v[44:45], v[36:37]
	s_nop 1
	v_mov_b32_dpp v46, v44 quad_perm:[1,0,3,2] row_mask:0xf bank_mask:0xf
	v_mov_b32_dpp v47, v45 quad_perm:[1,0,3,2] row_mask:0xf bank_mask:0xf
	v_add_f64 v[44:45], v[44:45], v[46:47]
	s_nop 1
	v_mov_b32_dpp v46, v44 quad_perm:[2,3,0,1] row_mask:0xf bank_mask:0xf
	v_mov_b32_dpp v47, v45 quad_perm:[2,3,0,1] row_mask:0xf bank_mask:0xf
	v_add_f64 v[44:45], v[44:45], v[46:47]
	s_nop 1
	v_mov_b32_dpp v46, v44 row_half_mirror row_mask:0xf bank_mask:0xf
	v_mov_b32_dpp v47, v45 row_half_mirror row_mask:0xf bank_mask:0xf
	v_add_f64 v[44:45], v[44:45], v[46:47]
	s_nop 1
	v_mov_b32_dpp v46, v44 row_mirror row_mask:0xf bank_mask:0xf
	v_mov_b32_dpp v47, v45 row_mirror row_mask:0xf bank_mask:0xf
	v_add_f64 v[44:45], v[44:45], v[46:47]
	s_nop 0
	v_readlane_b32 s10, v44, 0
	v_readlane_b32 s11, v45, 0
	v_readlane_b32 s12, v44, 16
	v_readlane_b32 s13, v45, 16
	v_readlane_b32 s14, v44, 32
	v_readlane_b32 s15, v45, 32
	v_readlane_b32 s16, v44, 48
	v_readlane_b32 s17, v45, 48
	v_cmp_eq_u32_e32 vcc, 0, v0
	s_and_saveexec_b64 s[2:3], vcc
	s_cbranch_execz .Lq_final_done
	v_mov_b32_e32 v0, s10
	v_mov_b32_e32 v1, s11
	v_add_f64 v[0:1], s[12:13], v[0:1]
	v_add_f64 v[0:1], s[14:15], v[0:1]
	v_add_f64 v[0:1], s[16:17], v[0:1]
	s_mov_b32 s2, 0
	s_mov_b32 s3, 0x415ec320
	v_div_scale_f64 v[4:5], s[8:9], s[2:3], s[2:3], v[0:1]
	v_rcp_f64_e32 v[6:7], v[4:5]
	s_nop 0
	v_fma_f64 v[8:9], -v[4:5], v[6:7], 1.0
	v_fmac_f64_e32 v[6:7], v[6:7], v[8:9]
	v_fma_f64 v[8:9], -v[4:5], v[6:7], 1.0
	v_fmac_f64_e32 v[6:7], v[6:7], v[8:9]
	v_div_scale_f64 v[8:9], vcc, v[0:1], s[2:3], v[0:1]
	v_mul_f64 v[10:11], v[8:9], v[6:7]
	v_fma_f64 v[4:5], -v[4:5], v[10:11], v[8:9]
	s_nop 1
	v_div_fmas_f64 v[4:5], v[4:5], v[6:7], v[10:11]
	v_div_fixup_f64 v[0:1], v[4:5], s[2:3], v[0:1]
	v_cvt_f32_f64_e32 v0, v[0:1]
	global_store_dword v3, v0, s[6:7]

	.amdhsa_kernel _Z10ssim_finalPKfPf
		.amdhsa_group_segment_fixed_size 0
		.amdhsa_private_segment_fixed_size 0
		.amdhsa_kernarg_size 16
		.amdhsa_user_sgpr_count 2
		.amdhsa_user_sgpr_dispatch_ptr 0
		.amdhsa_user_sgpr_queue_ptr 0
		.amdhsa_user_sgpr_kernarg_segment_ptr 1
		.amdhsa_user_sgpr_dispatch_id 0
		.amdhsa_user_sgpr_kernarg_preload_length 0
		.amdhsa_user_sgpr_kernarg_preload_offset 0
		.amdhsa_user_sgpr_private_segment_size 0
		.amdhsa_uses_dynamic_stack 0
		.amdhsa_enable_private_segment 0
		.amdhsa_system_sgpr_workgroup_id_x 1
		.amdhsa_system_sgpr_workgroup_id_y 0
		.amdhsa_system_sgpr_workgroup_id_z 0
		.amdhsa_system_sgpr_workgroup_info 0
		.amdhsa_system_vgpr_workitem_id 0
		.amdhsa_next_free_vgpr 53
		.amdhsa_next_free_sgpr 18
		.amdhsa_accum_offset 56
		.amdhsa_reserve_vcc 1
		.amdhsa_float_round_mode_32 0
		.amdhsa_float_round_mode_16_64 0
		.amdhsa_float_denorm_mode_32 3
		.amdhsa_float_denorm_mode_16_64 3
		.amdhsa_dx10_clamp 1
		.amdhsa_ieee_mode 1
		.amdhsa_fp16_overflow 0
		.amdhsa_tg_split 0
		.amdhsa_exception_fp_ieee_invalid_op 0
		.amdhsa_exception_fp_denorm_src 0
		.amdhsa_exception_fp_ieee_div_zero 0
		.amdhsa_exception_fp_ieee_overflow 0
		.amdhsa_exception_fp_ieee_underflow 0
		.amdhsa_exception_fp_ieee_inexact 0
		.amdhsa_exception_int_div_zero 0
	.end_amdhsa_kernel

amdhsa.kernels:
  - .agpr_count:     0
    .args:
      - .actual_access:  read_only
        .address_space:  global
        .offset:         0
        .size:           8
        .value_kind:     global_buffer
      - .actual_access:  read_only
        .address_space:  global
        .offset:         8
        .size:           8
        .value_kind:     global_buffer
      - .actual_access:  read_only
        .address_space:  global
        .offset:         16
        .size:           8
        .value_kind:     global_buffer
      - .actual_access:  write_only
        .address_space:  global
        .offset:         24
        .size:           8
        .value_kind:     global_buffer
    .group_segment_fixed_size: 145536
    .kernarg_segment_align: 8
    .kernarg_segment_size: 32
    .language:       OpenCL C
    .language_version:
      - 2
      - 0
    .max_flat_workgroup_size: 512
    .name:           _Z9ssim_mainPKfS0_S0_Pf
    .private_segment_fixed_size: 0
    .sgpr_count:     37
    .sgpr_spill_count: 0
    .symbol:         _Z9ssim_mainPKfS0_S0_Pf.kd
    .uniform_work_group_size: 1
    .uses_dynamic_stack: false
    .vgpr_count:     256
    .vgpr_spill_count: 0
    .wavefront_size: 64
  - .agpr_count:     0
    .args:
      - .actual_access:  read_only
        .address_space:  global
        .offset:         0
        .size:           8
        .value_kind:     global_buffer
      - .actual_access:  write_only
        .address_space:  global
        .offset:         8
        .size:           8
        .value_kind:     global_buffer
    .group_segment_fixed_size: 0
    .kernarg_segment_align: 8
    .kernarg_segment_size: 16
    .language:       OpenCL C
    .language_version:
      - 2
      - 0
    .max_flat_workgroup_size: 64
    .name:           _Z10ssim_finalPKfPf
    .private_segment_fixed_size: 0
    .sgpr_count:     24
    .sgpr_spill_count: 0
    .symbol:         _Z10ssim_finalPKfPf.kd
    .uniform_work_group_size: 1
    .uses_dynamic_stack: false
    .vgpr_count:     53
    .vgpr_spill_count: 0
    .wavefront_size: 64
